# prep low-rank RWKV projections (three [16x32]x[32x256] f32 products) moved from packed-f32 VALU to f32-operand MFMA, redistributed through wave-private LDS
# speedup vs baseline: 1.0193x; 1.0056x over previous
.LBB0_249:
	v_mov_b32_e32 v134, v12
	v_mov_b32_e32 v136, v90
	v_mov_b32_e32 v138, v102
	v_readfirstlane_b32 s2, v0
	v_and_b32_e32 v2, 15, v203
	v_lshrrev_b32_e32 v3, 4, v203
	s_lshr_b32 s2, s2, 6
	v_lshlrev_b32_e32 v4, 9, v2
	v_lshl_add_u32 v4, v3, 5, v4
	s_and_b32 s3, s2, 3
	s_lshl_b32 s3, s3, 8
	v_lshlrev_b32_e32 v5, 13, v3
	v_lshl_add_u32 v5, v2, 4, v5
	v_add_u32_e32 v5, s3, v5
	s_lshl_b32 s3, s2, 11
	s_add_i32 s3, s3, 0x1e000
	s_cmp_lt_u32 s2, 5
	s_cbranch_scc1 .Lmy_pp_a
	s_add_i32 s3, s3, 0xc00
.Lmy_pp_a:
	v_and_b32_e32 v34, 1, v3
	v_lshlrev_b32_e32 v34, 4, v34
	v_lshl_add_u32 v34, v2, 7, v34
	v_add_u32_e32 v34, s3, v34
	v_lshlrev_b32_e32 v110, 5, v203
	v_add_u32_e32 v110, s3, v110
	ds_read_b128 v[114:117], v4 offset:256
	ds_read_b128 v[118:121], v4 offset:272
	v_add_u32_e32 v108, 0x2000, v5
	ds_read_b128 v[122:125], v108 offset:0
	ds_read_b128 v[126:129], v108 offset:1024
	ds_read_b128 v[130:133], v108 offset:2048
	ds_read_b128 v[170:173], v108 offset:3072
	s_waitcnt lgkmcnt(0)
	v_mfma_f32_16x16x4_f32 v[6:9], v114, v122, 0
	v_mfma_f32_16x16x4_f32 v[10:13], v114, v123, 0
	v_mfma_f32_16x16x4_f32 v[14:17], v114, v124, 0
	v_mfma_f32_16x16x4_f32 v[94:97], v114, v125, 0
	v_mfma_f32_16x16x4_f32 v[6:9], v115, v126, v[6:9]
	v_mfma_f32_16x16x4_f32 v[10:13], v115, v127, v[10:13]
	v_mfma_f32_16x16x4_f32 v[14:17], v115, v128, v[14:17]
	v_mfma_f32_16x16x4_f32 v[94:97], v115, v129, v[94:97]
	v_mfma_f32_16x16x4_f32 v[6:9], v116, v130, v[6:9]
	v_mfma_f32_16x16x4_f32 v[10:13], v116, v131, v[10:13]
	v_mfma_f32_16x16x4_f32 v[14:17], v116, v132, v[14:17]
	v_mfma_f32_16x16x4_f32 v[94:97], v116, v133, v[94:97]
	v_mfma_f32_16x16x4_f32 v[6:9], v117, v170, v[6:9]
	v_mfma_f32_16x16x4_f32 v[10:13], v117, v171, v[10:13]
	v_mfma_f32_16x16x4_f32 v[14:17], v117, v172, v[14:17]
	v_mfma_f32_16x16x4_f32 v[94:97], v117, v173, v[94:97]
	s_nop 7
	ds_read_b128 v[122:125], v108 offset:4096
	ds_read_b128 v[126:129], v108 offset:5120
	ds_read_b128 v[130:133], v108 offset:6144
	ds_read_b128 v[170:173], v108 offset:7168
	s_waitcnt lgkmcnt(0)
	v_mfma_f32_16x16x4_f32 v[6:9], v118, v122, v[6:9]
	v_mfma_f32_16x16x4_f32 v[10:13], v118, v123, v[10:13]
	v_mfma_f32_16x16x4_f32 v[14:17], v118, v124, v[14:17]
	v_mfma_f32_16x16x4_f32 v[94:97], v118, v125, v[94:97]
	v_mfma_f32_16x16x4_f32 v[6:9], v119, v126, v[6:9]
	v_mfma_f32_16x16x4_f32 v[10:13], v119, v127, v[10:13]
	v_mfma_f32_16x16x4_f32 v[14:17], v119, v128, v[14:17]
	v_mfma_f32_16x16x4_f32 v[94:97], v119, v129, v[94:97]
	v_mfma_f32_16x16x4_f32 v[6:9], v120, v130, v[6:9]
	v_mfma_f32_16x16x4_f32 v[10:13], v120, v131, v[10:13]
	v_mfma_f32_16x16x4_f32 v[14:17], v120, v132, v[14:17]
	v_mfma_f32_16x16x4_f32 v[94:97], v120, v133, v[94:97]
	v_mfma_f32_16x16x4_f32 v[6:9], v121, v170, v[6:9]
	v_mfma_f32_16x16x4_f32 v[10:13], v121, v171, v[10:13]
	v_mfma_f32_16x16x4_f32 v[14:17], v121, v172, v[14:17]
	v_mfma_f32_16x16x4_f32 v[94:97], v121, v173, v[94:97]
	s_nop 7
	s_nop 15
	s_nop 15
	s_cmp_lt_u32 s2, 4
	s_cselect_b32 exec_lo, -1, 0
	s_cselect_b32 exec_hi, 0, -1
	ds_write_b128 v34, v[6:9] offset:0
	ds_write_b128 v34, v[10:13] offset:32
	ds_write_b128 v34, v[14:17] offset:64
	ds_write_b128 v34, v[94:97] offset:96
	s_mov_b64 exec, -1
	s_waitcnt lgkmcnt(0)
	ds_read_b128 v[174:177], v110
	ds_read_b128 v[178:181], v110 offset:16
	s_waitcnt lgkmcnt(0)
	ds_read_b128 v[114:117], v4 offset:0
	ds_read_b128 v[118:121], v4 offset:16
	v_add_u32_e32 v108, 0xa000, v5
	ds_read_b128 v[122:125], v108 offset:0
	ds_read_b128 v[126:129], v108 offset:1024
	ds_read_b128 v[130:133], v108 offset:2048
	ds_read_b128 v[170:173], v108 offset:3072
	s_waitcnt lgkmcnt(0)
	v_mfma_f32_16x16x4_f32 v[6:9], v114, v122, 0
	v_mfma_f32_16x16x4_f32 v[10:13], v114, v123, 0
	v_mfma_f32_16x16x4_f32 v[14:17], v114, v124, 0
	v_mfma_f32_16x16x4_f32 v[94:97], v114, v125, 0
	v_mfma_f32_16x16x4_f32 v[6:9], v115, v126, v[6:9]
	v_mfma_f32_16x16x4_f32 v[10:13], v115, v127, v[10:13]
	v_mfma_f32_16x16x4_f32 v[14:17], v115, v128, v[14:17]
	v_mfma_f32_16x16x4_f32 v[94:97], v115, v129, v[94:97]
	v_mfma_f32_16x16x4_f32 v[6:9], v116, v130, v[6:9]
	v_mfma_f32_16x16x4_f32 v[10:13], v116, v131, v[10:13]
	v_mfma_f32_16x16x4_f32 v[14:17], v116, v132, v[14:17]
	v_mfma_f32_16x16x4_f32 v[94:97], v116, v133, v[94:97]
	v_mfma_f32_16x16x4_f32 v[6:9], v117, v170, v[6:9]
	v_mfma_f32_16x16x4_f32 v[10:13], v117, v171, v[10:13]
	v_mfma_f32_16x16x4_f32 v[14:17], v117, v172, v[14:17]
	v_mfma_f32_16x16x4_f32 v[94:97], v117, v173, v[94:97]
	s_nop 7
	ds_read_b128 v[122:125], v108 offset:4096
	ds_read_b128 v[126:129], v108 offset:5120
	ds_read_b128 v[130:133], v108 offset:6144
	ds_read_b128 v[170:173], v108 offset:7168
	s_waitcnt lgkmcnt(0)
	v_mfma_f32_16x16x4_f32 v[6:9], v118, v122, v[6:9]
	v_mfma_f32_16x16x4_f32 v[10:13], v118, v123, v[10:13]
	v_mfma_f32_16x16x4_f32 v[14:17], v118, v124, v[14:17]
	v_mfma_f32_16x16x4_f32 v[94:97], v118, v125, v[94:97]
	v_mfma_f32_16x16x4_f32 v[6:9], v119, v126, v[6:9]
	v_mfma_f32_16x16x4_f32 v[10:13], v119, v127, v[10:13]
	v_mfma_f32_16x16x4_f32 v[14:17], v119, v128, v[14:17]
	v_mfma_f32_16x16x4_f32 v[94:97], v119, v129, v[94:97]
	v_mfma_f32_16x16x4_f32 v[6:9], v120, v130, v[6:9]
	v_mfma_f32_16x16x4_f32 v[10:13], v120, v131, v[10:13]
	v_mfma_f32_16x16x4_f32 v[14:17], v120, v132, v[14:17]
	v_mfma_f32_16x16x4_f32 v[94:97], v120, v133, v[94:97]
	v_mfma_f32_16x16x4_f32 v[6:9], v121, v170, v[6:9]
	v_mfma_f32_16x16x4_f32 v[10:13], v121, v171, v[10:13]
	v_mfma_f32_16x16x4_f32 v[14:17], v121, v172, v[14:17]
	v_mfma_f32_16x16x4_f32 v[94:97], v121, v173, v[94:97]
	s_nop 7
	s_nop 15
	s_nop 15
	s_cmp_lt_u32 s2, 4
	s_cselect_b32 exec_lo, -1, 0
	s_cselect_b32 exec_hi, 0, -1
	ds_write_b128 v34, v[6:9] offset:0
	ds_write_b128 v34, v[10:13] offset:32
	ds_write_b128 v34, v[14:17] offset:64
	ds_write_b128 v34, v[94:97] offset:96
	s_mov_b64 exec, -1
	s_waitcnt lgkmcnt(0)
	ds_read_b128 v[182:185], v110
	ds_read_b128 v[186:189], v110 offset:16
	s_waitcnt lgkmcnt(0)
	ds_read_b128 v[114:117], v4 offset:128
	ds_read_b128 v[118:121], v4 offset:144
	v_add_u32_e32 v108, 0x12000, v5
	ds_read_b128 v[122:125], v108 offset:0
	ds_read_b128 v[126:129], v108 offset:1024
	ds_read_b128 v[130:133], v108 offset:2048
	ds_read_b128 v[170:173], v108 offset:3072
	s_waitcnt lgkmcnt(0)
	v_mfma_f32_16x16x4_f32 v[6:9], v114, v122, 0
	v_mfma_f32_16x16x4_f32 v[10:13], v114, v123, 0
	v_mfma_f32_16x16x4_f32 v[14:17], v114, v124, 0
	v_mfma_f32_16x16x4_f32 v[94:97], v114, v125, 0
	v_mfma_f32_16x16x4_f32 v[6:9], v115, v126, v[6:9]
	v_mfma_f32_16x16x4_f32 v[10:13], v115, v127, v[10:13]
	v_mfma_f32_16x16x4_f32 v[14:17], v115, v128, v[14:17]
	v_mfma_f32_16x16x4_f32 v[94:97], v115, v129, v[94:97]
	v_mfma_f32_16x16x4_f32 v[6:9], v116, v130, v[6:9]
	v_mfma_f32_16x16x4_f32 v[10:13], v116, v131, v[10:13]
	v_mfma_f32_16x16x4_f32 v[14:17], v116, v132, v[14:17]
	v_mfma_f32_16x16x4_f32 v[94:97], v116, v133, v[94:97]
	v_mfma_f32_16x16x4_f32 v[6:9], v117, v170, v[6:9]
	v_mfma_f32_16x16x4_f32 v[10:13], v117, v171, v[10:13]
	v_mfma_f32_16x16x4_f32 v[14:17], v117, v172, v[14:17]
	v_mfma_f32_16x16x4_f32 v[94:97], v117, v173, v[94:97]
	s_nop 7
	ds_read_b128 v[122:125], v108 offset:4096
	ds_read_b128 v[126:129], v108 offset:5120
	ds_read_b128 v[130:133], v108 offset:6144
	ds_read_b128 v[170:173], v108 offset:7168
	s_waitcnt lgkmcnt(0)
	v_mfma_f32_16x16x4_f32 v[6:9], v118, v122, v[6:9]
	v_mfma_f32_16x16x4_f32 v[10:13], v118, v123, v[10:13]
	v_mfma_f32_16x16x4_f32 v[14:17], v118, v124, v[14:17]
	v_mfma_f32_16x16x4_f32 v[94:97], v118, v125, v[94:97]
	v_mfma_f32_16x16x4_f32 v[6:9], v119, v126, v[6:9]
	v_mfma_f32_16x16x4_f32 v[10:13], v119, v127, v[10:13]
	v_mfma_f32_16x16x4_f32 v[14:17], v119, v128, v[14:17]
	v_mfma_f32_16x16x4_f32 v[94:97], v119, v129, v[94:97]
	v_mfma_f32_16x16x4_f32 v[6:9], v120, v130, v[6:9]
	v_mfma_f32_16x16x4_f32 v[10:13], v120, v131, v[10:13]
	v_mfma_f32_16x16x4_f32 v[14:17], v120, v132, v[14:17]
	v_mfma_f32_16x16x4_f32 v[94:97], v120, v133, v[94:97]
	v_mfma_f32_16x16x4_f32 v[6:9], v121, v170, v[6:9]
	v_mfma_f32_16x16x4_f32 v[10:13], v121, v171, v[10:13]
	v_mfma_f32_16x16x4_f32 v[14:17], v121, v172, v[14:17]
	v_mfma_f32_16x16x4_f32 v[94:97], v121, v173, v[94:97]
	s_nop 7
	s_nop 15
	s_nop 15
	s_cmp_lt_u32 s2, 4
	s_cselect_b32 exec_lo, -1, 0
	s_cselect_b32 exec_hi, 0, -1
	ds_write_b128 v34, v[6:9] offset:0
	ds_write_b128 v34, v[10:13] offset:32
	ds_write_b128 v34, v[14:17] offset:64
	ds_write_b128 v34, v[94:97] offset:96
	s_mov_b64 exec, -1
	s_waitcnt lgkmcnt(0)
	ds_read_b128 v[122:125], v110
	ds_read_b128 v[126:129], v110 offset:16
	s_waitcnt lgkmcnt(0)
	v_add_f32_e32 v102, v138, v174
	v_add_f32_e32 v103, v138, v175
	v_add_f32_e32 v16, v138, v176
	v_add_f32_e32 v17, v138, v177
	v_add_f32_e32 v10, v138, v178
	v_add_f32_e32 v11, v138, v179
	v_add_f32_e32 v96, v138, v180
	v_add_f32_e32 v97, v138, v181
	v_add_f32_e32 v107, v134, v182
	v_add_f32_e32 v106, v134, v183
	v_add_f32_e32 v13, v134, v184
	v_add_f32_e32 v12, v134, v185
	v_add_f32_e32 v8, v134, v186
	v_add_f32_e32 v9, v134, v187
	v_add_f32_e32 v94, v134, v188
	v_add_f32_e32 v95, v134, v189
	v_add_f32_e32 v105, v136, v122
	v_add_f32_e32 v104, v136, v123
	v_add_f32_e32 v15, v136, v124
	v_add_f32_e32 v14, v136, v125
	v_add_f32_e32 v7, v136, v126
	v_add_f32_e32 v6, v136, v127
	v_add_f32_e32 v91, v136, v128
	v_add_f32_e32 v90, v136, v129
	s_mov_b32 s2, 0
	v_lshlrev_b32_e32 v2, 16, v157
	v_cndmask_b32_e64 v123, 0, v2, s[40:41]
	v_lshlrev_b32_e32 v2, 16, v154
	v_cndmask_b32_e32 v126, 0, v2, vcc
	v_lshlrev_b32_e32 v2, 16, v152
	v_cndmask_b32_e32 v127, 0, v2, vcc
	global_load_dword v2, v[32:33], off offset:1024
	global_load_dword v3, v[40:41], off
	global_load_dword v4, v[36:37], off
	global_load_dword v5, v[38:39], off
	global_load_dword v110, v[32:33], off offset:3712
	global_load_dword v108, v[32:33], off offset:2048
	global_load_dword v112, v[32:33], off
	v_lshlrev_b32_e32 v34, 16, v160
	v_cndmask_b32_e64 v128, 0, v34, s[42:43]
	v_lshlrev_b32_e32 v81, 16, v81
	v_lshlrev_b32_e32 v34, 16, v83
	v_cndmask_b32_e32 v129, 0, v34, vcc
	v_lshlrev_b32_e32 v34, 16, v144
	v_cndmask_b32_e32 v144, 0, v81, vcc
	global_load_dword v81, v[42:43], off
	v_lshlrev_b32_e32 v116, 16, v153
	v_cndmask_b32_e64 v130, 0, v34, s[44:45]
	v_lshlrev_b32_e32 v34, 16, v109
	v_lshlrev_b32_e32 v89, 16, v89
	v_lshlrev_b32_e32 v114, 16, v156
	v_cndmask_b32_e64 v83, 0, v34, s[46:47]
	v_lshlrev_b32_e32 v34, 16, v93
	v_lshlrev_b32_e32 v93, 16, v99
	v_cndmask_b32_e32 v133, 0, v116, vcc
	v_cndmask_b32_e64 v116, 0, v89, s[48:49]
	v_and_b32_e32 v89, 64, v203
	v_lshlrev_b32_e32 v117, 16, v155
	v_lshlrev_b32_e32 v118, 16, v151
	v_lshlrev_b32_e32 v119, 16, v161
	v_lshlrev_b32_e32 v85, 16, v85
	v_lshlrev_b32_e32 v79, 16, v79
	v_lshlrev_b32_e32 v109, 16, v111
	v_cndmask_b32_e64 v111, 0, v34, s[48:49]
	v_lshlrev_b32_e32 v99, 16, v148
	v_lshlrev_b32_e32 v34, 16, v149
	v_lshlrev_b32_e32 v122, 16, v150
	v_cndmask_b32_e64 v131, 0, v114, s[40:41]
	v_cndmask_b32_e64 v114, 0, v93, s[48:49]
	v_add_u32_e32 v89, 64, v89
	v_xor_b32_e32 v93, 1, v203
	v_cndmask_b32_e32 v34, 0, v34, vcc
	v_lshlrev_b32_e32 v124, 16, v145
	v_cndmask_b32_e32 v134, 0, v117, vcc
	v_cndmask_b32_e32 v136, 0, v118, vcc
	v_cndmask_b32_e32 v138, 0, v119, vcc
	v_cndmask_b32_e32 v85, 0, v85, vcc
	v_cndmask_b32_e64 v145, 0, v79, s[44:45]
	v_cndmask_b32_e64 v148, 0, v109, s[46:47]
	v_cndmask_b32_e32 v109, 0, v99, vcc
	v_cndmask_b32_e32 v79, 0, v122, vcc
	v_cmp_lt_i32_e32 vcc, v93, v89
	v_lshlrev_b32_e32 v121, 16, v113
	v_lshlrev_b32_e32 v113, 16, v146
	v_cndmask_b32_e32 v93, v203, v93, vcc
	v_lshlrev_b32_e32 v122, 2, v93
	v_xor_b32_e32 v93, 2, v203
	v_cmp_lt_i32_e32 vcc, v93, v89
	v_cndmask_b32_e64 v146, 0, v121, s[44:45]
	v_lshlrev_b32_e32 v120, 16, v159
	v_cndmask_b32_e32 v93, v203, v93, vcc
	v_lshlrev_b32_e32 v121, 2, v93
	v_xor_b32_e32 v93, 4, v203
	v_cmp_lt_i32_e32 vcc, v93, v89
	v_cndmask_b32_e64 v140, 0, v120, s[42:43]
	v_sub_f32_e32 v99, v127, v126
	v_cndmask_b32_e32 v93, v203, v93, vcc
	v_lshlrev_b32_e32 v120, 2, v93
	v_xor_b32_e32 v93, 8, v203
	v_cmp_lt_i32_e32 vcc, v93, v89
	v_lshlrev_b32_e32 v101, 16, v101
	v_lshlrev_b32_e32 v125, 16, v147
	v_cndmask_b32_e32 v93, v203, v93, vcc
	v_lshlrev_b32_e32 v119, 2, v93
	v_xor_b32_e32 v93, 16, v203
	v_cmp_lt_i32_e32 vcc, v93, v89
	v_cndmask_b32_e64 v147, 0, v101, s[46:47]
	v_lshlrev_b32_e32 v115, 16, v158
	v_cndmask_b32_e32 v93, v203, v93, vcc
	v_lshlrev_b32_e32 v118, 2, v93
	v_xor_b32_e32 v93, 32, v203
	v_cmp_lt_i32_e32 vcc, v93, v89
	v_cndmask_b32_e64 v132, 0, v115, s[40:41]
	v_cndmask_b32_e64 v115, 0, v125, s[50:51]
	v_cndmask_b32_e32 v89, v203, v93, vcc
	v_sub_f32_e32 v93, v123, v126
	s_waitcnt vmcnt(7)
	v_fma_f32 v93, v93, v2, v126
	s_waitcnt vmcnt(5)
	v_fmac_f32_e32 v93, v99, v4
	v_mul_f32_e32 v99, v93, v3
	v_mul_f32_e32 v101, v99, v99
	s_nop 1
	v_mov_b32_dpp v101, v101 quad_perm:[1,0,3,2] row_mask:0xf bank_mask:0xf
	v_lshlrev_b32_e32 v123, 2, v89
	v_sub_f32_e32 v89, v131, v133
	v_cndmask_b32_e64 v117, 0, v124, s[50:51]
	s_waitcnt vmcnt(1)
	v_fma_f32 v89, v89, v112, v133
	s_waitcnt lgkmcnt(0)
	v_fmac_f32_e32 v101, v99, v99
	s_nop 1
	v_mov_b32_dpp v125, v101 quad_perm:[2,3,0,1] row_mask:0xf bank_mask:0xf
	v_sub_f32_e32 v124, v136, v133
	v_fmac_f32_e32 v89, v124, v110
	v_sub_f32_e32 v124, v132, v134
	v_fma_f32 v131, v124, v108, v134
	s_waitcnt lgkmcnt(0)
	v_add_f32_e32 v101, v101, v125
	s_nop 1
	v_mov_b32_dpp v125, v101 row_half_mirror row_mask:0xf bank_mask:0xf
	v_sub_f32_e32 v124, v138, v134
	v_fmac_f32_e32 v131, v124, v5
	v_mul_f32_e32 v102, 0xbfb8aa3b, v102
	v_exp_f32_e32 v102, v102
	s_waitcnt lgkmcnt(0)
	v_add_f32_e32 v101, v101, v125
	s_nop 1
	v_mov_b32_dpp v125, v101 row_mirror row_mask:0xf bank_mask:0xf
	v_mul_f32_e32 v107, 0xbfb8aa3b, v107
	v_add_f32_e32 v102, 1.0, v102
	v_rcp_f32_e32 v102, v102
	v_exp_f32_e32 v107, v107
	s_waitcnt lgkmcnt(0)
	v_add_f32_e32 v101, v101, v125
	v_mov_b32_e32 v124, v101
	s_nop 1
	v_permlane16_swap_b32_e32 v124, v101
	v_mul_f32_e32 v105, 0xbfb8aa3b, v105
	v_exp_f32_e32 v105, v105
	v_cvt_pk_bf16_f32 v89, v89, s0
	v_add_f32_e32 v107, 1.0, v107
	s_waitcnt lgkmcnt(0)
	v_add_f32_e32 v101, v101, v124
	v_mov_b32_e32 v124, v101
	s_nop 1
	v_permlane32_swap_b32_e32 v124, v101
	v_rcp_f32_e32 v107, v107
	v_add_f32_e32 v105, 1.0, v105
	v_rcp_f32_e32 v105, v105
	v_mul_f32_e32 v103, 0xbfb8aa3b, v103
	s_waitcnt lgkmcnt(0)
	v_add_f32_e32 v101, v101, v124
	v_add_f32_e32 v101, 0x2b8cbccc, v101
	v_rsq_f32_e32 v101, v101
	v_mul_f32_e32 v107, 0xbf1b459e, v107
	v_mul_f32_e32 v107, 0x3fb8aa3b, v107
	v_mul_f32_e32 v105, 0xbf1b459e, v105
	v_mul_f32_e32 v99, v99, v101
	v_add_f32_e32 v101, -1.0, v102
	s_waitcnt vmcnt(0)
	v_fma_f32 v101, v101, v81, 1.0
	v_mul_f32_e32 v93, v93, v101
	v_ashrrev_i32_e32 v101, 31, v100
	v_lshlrev_b64 v[100:101], 9, v[100:101]
	v_or_b32_e32 v100, v100, v31
	v_lshl_add_u64 v[124:125], s[74:75], 0, v[100:101]
	global_store_short v[124:125], v89, off
	v_lshl_add_u64 v[124:125], s[76:77], 0, v[100:101]
	v_cvt_pk_bf16_f32 v89, v93, s0
	global_store_short v[124:125], v89, off
	v_lshl_add_u64 v[124:125], s[78:79], 0, v[100:101]
	v_cvt_pk_bf16_f32 v89, v131, s0
	global_store_short v[124:125], v89, off
	v_lshl_add_u64 v[124:125], s[80:81], 0, v[100:101]
	v_cvt_pk_bf16_f32 v89, v99, s0
	v_sub_f32_e32 v93, v126, v127
	global_store_short v[124:125], v89, off
	v_mul_f32_e32 v89, v102, v99
	v_fma_f32 v93, v93, v2, v127
	v_sub_f32_e32 v99, v128, v127
	v_fmac_f32_e32 v93, v99, v4
	v_mul_f32_e32 v99, v93, v3
	v_mul_f32_e32 v102, v99, v99
	v_exp_f32_e32 v107, v107
	v_mul_f32_e32 v105, 0x3fb8aa3b, v105
	s_nop 1
	v_mov_b32_dpp v102, v102 quad_perm:[1,0,3,2] row_mask:0xf bank_mask:0xf
	v_exp_f32_e32 v105, v105
	v_lshl_add_u64 v[124:125], s[82:83], 0, v[100:101]
	v_cvt_pk_bf16_f32 v89, v89, s0
	global_store_short v[124:125], v89, off
	v_lshl_add_u64 v[124:125], s[84:85], 0, v[100:101]
	v_cvt_pk_bf16_f32 v89, v107, s0
	global_store_short v[124:125], v89, off
	v_lshl_add_u64 v[100:101], s[86:87], 0, v[100:101]
	v_cvt_pk_bf16_f32 v89, v105, s0
	s_waitcnt lgkmcnt(0)
	v_fmac_f32_e32 v102, v99, v99
	global_store_short v[100:101], v89, off
	s_nop 1
	v_mov_b32_dpp v101, v102 quad_perm:[2,3,0,1] row_mask:0xf bank_mask:0xf
	v_mul_f32_e32 v106, 0xbfb8aa3b, v106
	v_sub_f32_e32 v89, v133, v136
	v_exp_f32_e32 v103, v103
	v_exp_f32_e32 v106, v106
	s_waitcnt lgkmcnt(0)
	v_add_f32_e32 v101, v102, v101
	s_nop 1
	v_mov_b32_dpp v102, v101 row_half_mirror row_mask:0xf bank_mask:0xf
	v_lshlrev_b32_e32 v87, 16, v87
	v_fma_f32 v89, v89, v112, v136
	v_sub_f32_e32 v100, v140, v136
	v_cndmask_b32_e64 v87, 0, v87, s[42:43]
	s_waitcnt lgkmcnt(0)
	v_add_f32_e32 v101, v101, v102
	s_nop 1
	v_mov_b32_dpp v102, v101 row_mirror row_mask:0xf bank_mask:0xf
	v_fmac_f32_e32 v89, v100, v110
	v_sub_f32_e32 v100, v134, v138
	v_fma_f32 v105, v100, v108, v138
	v_sub_f32_e32 v100, v87, v138
	s_waitcnt lgkmcnt(0)
	v_add_f32_e32 v101, v101, v102
	v_mov_b32_e32 v102, v101
	s_nop 1
	v_permlane16_swap_b32_e32 v102, v101
	v_fmac_f32_e32 v105, v100, v5
	v_add_f32_e32 v100, 1.0, v103
	v_add_f32_e32 v103, 1.0, v106
	v_rcp_f32_e32 v103, v103
	s_waitcnt lgkmcnt(0)
	v_add_f32_e32 v101, v101, v102
	v_mov_b32_e32 v102, v101
	s_nop 1
	v_permlane32_swap_b32_e32 v102, v101
	v_rcp_f32_e32 v106, v100
	v_mul_f32_e32 v100, 0xbf1b459e, v103
	v_mul_f32_e32 v103, 0xbfb8aa3b, v104
	v_exp_f32_e32 v103, v103
	s_waitcnt lgkmcnt(0)
	v_add_f32_e32 v101, v101, v102
	v_add_f32_e32 v101, 0x2b8cbccc, v101
	v_rsq_f32_e32 v101, v101
	v_mul_f32_e32 v100, 0x3fb8aa3b, v100
	v_exp_f32_e32 v104, v100
	v_add_f32_e32 v100, 1.0, v103
	v_rcp_f32_e32 v100, v100
	v_mul_f32_e32 v103, v99, v101
	v_add_f32_e32 v99, -1.0, v106
	v_fma_f32 v99, v99, v81, 1.0
	v_mul_f32_e32 v93, v93, v99
	v_ashrrev_i32_e32 v99, 31, v98
	v_mul_f32_e32 v100, 0xbf1b459e, v100
	v_lshlrev_b64 v[98:99], 9, v[98:99]
	v_mul_f32_e32 v100, 0x3fb8aa3b, v100
	v_or_b32_e32 v98, v98, v31
	v_exp_f32_e32 v102, v100
	v_lshl_add_u64 v[100:101], s[74:75], 0, v[98:99]
	v_cvt_pk_bf16_f32 v89, v89, s0
	global_store_short v[100:101], v89, off
	v_lshl_add_u64 v[100:101], s[76:77], 0, v[98:99]
	v_cvt_pk_bf16_f32 v89, v93, s0
	global_store_short v[100:101], v89, off
	v_lshl_add_u64 v[100:101], s[78:79], 0, v[98:99]
	v_cvt_pk_bf16_f32 v89, v105, s0
	global_store_short v[100:101], v89, off
	v_lshl_add_u64 v[100:101], s[80:81], 0, v[98:99]
	v_cvt_pk_bf16_f32 v89, v103, s0
	global_store_short v[100:101], v89, off
	v_mul_f32_e32 v89, v106, v103
	v_lshl_add_u64 v[100:101], s[82:83], 0, v[98:99]
	v_cvt_pk_bf16_f32 v89, v89, s0
	global_store_short v[100:101], v89, off
	v_lshl_add_u64 v[100:101], s[84:85], 0, v[98:99]
	v_cvt_pk_bf16_f32 v89, v104, s0
	v_sub_f32_e32 v93, v127, v128
	global_store_short v[100:101], v89, off
	v_fma_f32 v93, v93, v2, v128
	v_sub_f32_e32 v100, v129, v128
	v_fmac_f32_e32 v93, v100, v4
	v_mul_f32_e32 v100, v93, v3
	v_mul_f32_e32 v101, v100, v100
	s_nop 1
	v_mov_b32_dpp v101, v101 quad_perm:[1,0,3,2] row_mask:0xf bank_mask:0xf
	v_lshl_add_u64 v[98:99], s[86:87], 0, v[98:99]
	v_cvt_pk_bf16_f32 v89, v102, s0
	global_store_short v[98:99], v89, off
	v_sub_f32_e32 v89, v136, v140
	s_waitcnt lgkmcnt(0)
	v_fmac_f32_e32 v101, v100, v100
	s_nop 1
	v_mov_b32_dpp v99, v101 quad_perm:[2,3,0,1] row_mask:0xf bank_mask:0xf
	v_fma_f32 v89, v89, v112, v140
	v_sub_f32_e32 v98, v144, v140
	v_fmac_f32_e32 v89, v98, v110
	v_sub_f32_e32 v98, v138, v87
	s_waitcnt lgkmcnt(0)
	v_add_f32_e32 v99, v101, v99
	s_nop 1
	v_mov_b32_dpp v101, v99 row_half_mirror row_mask:0xf bank_mask:0xf
	v_fma_f32 v102, v98, v108, v87
	v_sub_f32_e32 v98, v85, v87
	v_fmac_f32_e32 v102, v98, v5
	v_mul_f32_e32 v16, 0xbfb8aa3b, v16
	s_waitcnt lgkmcnt(0)
	v_add_f32_e32 v99, v99, v101
	s_nop 1
	v_mov_b32_dpp v101, v99 row_mirror row_mask:0xf bank_mask:0xf
	v_exp_f32_e32 v16, v16
	v_mul_f32_e32 v13, 0xbfb8aa3b, v13
	v_exp_f32_e32 v13, v13
	v_mul_f32_e32 v15, 0xbfb8aa3b, v15
	s_waitcnt lgkmcnt(0)
	v_add_f32_e32 v98, v99, v101
	v_mov_b32_e32 v99, v98
	s_nop 1
	v_permlane16_swap_b32_e32 v99, v98
	v_add_f32_e32 v16, 1.0, v16
	v_rcp_f32_e32 v16, v16
	v_exp_f32_e32 v15, v15
	v_add_f32_e32 v13, 1.0, v13
	s_waitcnt lgkmcnt(0)
	v_add_f32_e32 v98, v98, v99
	v_mov_b32_e32 v99, v98
	s_nop 1
	v_permlane32_swap_b32_e32 v99, v98
	v_rcp_f32_e32 v13, v13
	v_add_f32_e32 v15, 1.0, v15
	v_rcp_f32_e32 v15, v15
	v_cvt_pk_bf16_f32 v89, v89, s0
	s_waitcnt lgkmcnt(0)
	v_add_f32_e32 v98, v98, v99
	v_add_f32_e32 v98, 0x2b8cbccc, v98
	v_rsq_f32_e32 v98, v98
	v_mul_f32_e32 v13, 0xbf1b459e, v13
	v_mul_f32_e32 v13, 0x3fb8aa3b, v13
	v_mul_f32_e32 v15, 0xbf1b459e, v15
	v_mul_f32_e32 v100, v100, v98
	v_add_f32_e32 v98, -1.0, v16
	v_fma_f32 v98, v98, v81, 1.0
	v_mul_f32_e32 v101, v93, v98
	v_ashrrev_i32_e32 v93, 31, v92
	v_lshlrev_b64 v[92:93], 9, v[92:93]
	v_or_b32_e32 v92, v92, v31
	v_lshl_add_u64 v[98:99], s[74:75], 0, v[92:93]
	v_exp_f32_e32 v13, v13
	v_mul_f32_e32 v15, 0x3fb8aa3b, v15
	global_store_short v[98:99], v89, off
	v_lshl_add_u64 v[98:99], s[76:77], 0, v[92:93]
	v_cvt_pk_bf16_f32 v89, v101, s0
	v_exp_f32_e32 v15, v15
	global_store_short v[98:99], v89, off
	v_lshl_add_u64 v[98:99], s[78:79], 0, v[92:93]
	v_cvt_pk_bf16_f32 v89, v102, s0
	global_store_short v[98:99], v89, off
	v_lshl_add_u64 v[98:99], s[80:81], 0, v[92:93]
	v_cvt_pk_bf16_f32 v89, v100, s0
	v_mul_f32_e32 v16, v16, v100
	global_store_short v[98:99], v89, off
	v_lshl_add_u64 v[98:99], s[82:83], 0, v[92:93]
	v_cvt_pk_bf16_f32 v16, v16, s0
	global_store_short v[98:99], v16, off
	v_lshl_add_u64 v[98:99], s[84:85], 0, v[92:93]
	v_cvt_pk_bf16_f32 v13, v13, s0
	global_store_short v[98:99], v13, off
	v_cvt_pk_bf16_f32 v13, v15, s0
	v_sub_f32_e32 v15, v128, v129
	v_fma_f32 v15, v15, v2, v129
	v_sub_f32_e32 v16, v130, v129
	v_fmac_f32_e32 v15, v16, v4
	v_mul_f32_e32 v16, v15, v3
	v_mul_f32_e32 v89, v16, v16
	s_nop 1
	v_mov_b32_dpp v89, v89 quad_perm:[1,0,3,2] row_mask:0xf bank_mask:0xf
	v_lshl_add_u64 v[92:93], s[86:87], 0, v[92:93]
	global_store_short v[92:93], v13, off
	v_sub_f32_e32 v13, v140, v144
	v_fma_f32 v92, v13, v112, v144
	s_waitcnt lgkmcnt(0)
	v_fmac_f32_e32 v89, v16, v16
	s_nop 1
	v_mov_b32_dpp v93, v89 quad_perm:[2,3,0,1] row_mask:0xf bank_mask:0xf
	v_sub_f32_e32 v13, v145, v144
	v_fmac_f32_e32 v92, v13, v110
	v_sub_f32_e32 v13, v87, v85
	v_mul_f32_e32 v17, 0xbfb8aa3b, v17
	s_waitcnt lgkmcnt(0)
	v_add_f32_e32 v87, v89, v93
	s_nop 1
	v_mov_b32_dpp v89, v87 row_half_mirror row_mask:0xf bank_mask:0xf
	v_exp_f32_e32 v17, v17
	v_mul_f32_e32 v12, 0xbfb8aa3b, v12
	v_exp_f32_e32 v12, v12
	v_fma_f32 v98, v13, v108, v85
	s_waitcnt lgkmcnt(0)
	v_add_f32_e32 v87, v87, v89
	s_nop 1
	v_mov_b32_dpp v89, v87 row_mirror row_mask:0xf bank_mask:0xf
	v_sub_f32_e32 v13, v146, v85
	v_fmac_f32_e32 v98, v13, v5
	v_add_f32_e32 v13, 1.0, v17
	v_add_f32_e32 v12, 1.0, v12
	s_waitcnt lgkmcnt(0)
	v_add_f32_e32 v17, v87, v89
	v_mov_b32_e32 v87, v17
	s_nop 1
	v_permlane16_swap_b32_e32 v87, v17
	v_rcp_f32_e32 v12, v12
	v_rcp_f32_e32 v89, v13
	v_mul_f32_e32 v13, 0xbfb8aa3b, v14
	v_exp_f32_e32 v13, v13
	s_waitcnt lgkmcnt(0)
	v_add_f32_e32 v14, v17, v87
	v_mul_f32_e32 v12, 0xbf1b459e, v12
	v_mov_b32_e32 v17, v14
	s_nop 1
	v_permlane32_swap_b32_e32 v17, v14
	v_mul_f32_e32 v12, 0x3fb8aa3b, v12
	v_exp_f32_e32 v93, v12
	v_add_f32_e32 v12, 1.0, v13
	v_rcp_f32_e32 v12, v12
	s_waitcnt lgkmcnt(0)
	v_add_f32_e32 v13, v14, v17
	v_add_f32_e32 v13, 0x2b8cbccc, v13
	v_rsq_f32_e32 v13, v13
	v_mul_f32_e32 v12, 0xbf1b459e, v12
	v_mul_f32_e32 v12, 0x3fb8aa3b, v12
	v_exp_f32_e32 v17, v12
	v_add_f32_e32 v12, -1.0, v89
	v_fma_f32 v12, v12, v81, 1.0
	v_ashrrev_i32_e32 v87, 31, v86
	v_mul_f32_e32 v16, v16, v13
	v_mul_f32_e32 v99, v15, v12
	v_lshlrev_b64 v[12:13], 9, v[86:87]
	v_or_b32_e32 v12, v12, v31
	v_lshl_add_u64 v[14:15], s[74:75], 0, v[12:13]
	v_cvt_pk_bf16_f32 v86, v92, s0
	global_store_short v[14:15], v86, off
	v_lshl_add_u64 v[14:15], s[76:77], 0, v[12:13]
	v_cvt_pk_bf16_f32 v86, v99, s0
	global_store_short v[14:15], v86, off
	v_lshl_add_u64 v[14:15], s[78:79], 0, v[12:13]
	v_cvt_pk_bf16_f32 v86, v98, s0
	global_store_short v[14:15], v86, off
	v_lshl_add_u64 v[14:15], s[80:81], 0, v[12:13]
	v_cvt_pk_bf16_f32 v86, v16, s0
	v_mul_f32_e32 v16, v89, v16
	global_store_short v[14:15], v86, off
	v_lshl_add_u64 v[14:15], s[82:83], 0, v[12:13]
	v_cvt_pk_bf16_f32 v16, v16, s0
	global_store_short v[14:15], v16, off
	v_lshl_add_u64 v[14:15], s[84:85], 0, v[12:13]
	v_cvt_pk_bf16_f32 v16, v93, s0
	global_store_short v[14:15], v16, off
	v_sub_f32_e32 v15, v129, v130
	v_fma_f32 v15, v15, v2, v130
	v_sub_f32_e32 v16, v83, v130
	v_fmac_f32_e32 v15, v16, v4
	v_mul_f32_e32 v16, v15, v3
	v_cvt_pk_bf16_f32 v14, v17, s0
	v_mul_f32_e32 v17, v16, v16
	s_nop 1
	v_mov_b32_dpp v17, v17 quad_perm:[1,0,3,2] row_mask:0xf bank_mask:0xf
	v_lshl_add_u64 v[12:13], s[86:87], 0, v[12:13]
	global_store_short v[12:13], v14, off
	v_sub_f32_e32 v12, v144, v145
	v_fma_f32 v86, v12, v112, v145
	s_waitcnt lgkmcnt(0)
	v_fmac_f32_e32 v17, v16, v16
	s_nop 1
	v_mov_b32_dpp v13, v17 quad_perm:[2,3,0,1] row_mask:0xf bank_mask:0xf
	v_sub_f32_e32 v12, v147, v145
	v_fmac_f32_e32 v86, v12, v110
	v_sub_f32_e32 v12, v85, v146
	v_fma_f32 v85, v12, v108, v146
	s_waitcnt lgkmcnt(0)
	v_add_f32_e32 v13, v17, v13
	s_nop 1
	v_mov_b32_dpp v14, v13 row_half_mirror row_mask:0xf bank_mask:0xf
	v_sub_f32_e32 v12, v148, v146
	v_fmac_f32_e32 v85, v12, v5
	v_mul_f32_e32 v10, 0xbfb8aa3b, v10
	v_exp_f32_e32 v10, v10
	s_waitcnt lgkmcnt(0)
	v_add_f32_e32 v13, v13, v14
	s_nop 1
	v_mov_b32_dpp v14, v13 row_mirror row_mask:0xf bank_mask:0xf
	v_mul_f32_e32 v8, 0xbfb8aa3b, v8
	v_exp_f32_e32 v8, v8
	v_add_f32_e32 v10, 1.0, v10
	v_rcp_f32_e32 v10, v10
	s_waitcnt lgkmcnt(0)
	v_add_f32_e32 v12, v13, v14
	v_mov_b32_e32 v13, v12
	s_nop 1
	v_permlane16_swap_b32_e32 v13, v12
	v_add_f32_e32 v8, 1.0, v8
	v_rcp_f32_e32 v8, v8
	v_ashrrev_i32_e32 v89, 31, v88
	v_mul_f32_e32 v7, 0xbfb8aa3b, v7
	s_waitcnt lgkmcnt(0)
	v_add_f32_e32 v12, v12, v13
	v_mov_b32_e32 v13, v12
	s_nop 1
	v_permlane32_swap_b32_e32 v13, v12
	v_mul_f32_e32 v8, 0xbf1b459e, v8
	v_mul_f32_e32 v8, 0x3fb8aa3b, v8
	v_cvt_pk_bf16_f32 v86, v86, s0
	v_exp_f32_e32 v7, v7
	s_waitcnt lgkmcnt(0)
	v_add_f32_e32 v12, v12, v13
	v_add_f32_e32 v12, 0x2b8cbccc, v12
	v_rsq_f32_e32 v12, v12
	v_exp_f32_e32 v8, v8
	v_add_f32_e32 v7, 1.0, v7
	v_rcp_f32_e32 v7, v7
	v_mul_f32_e32 v16, v16, v12
	v_add_f32_e32 v12, -1.0, v10
	v_fma_f32 v12, v12, v81, 1.0
	v_mul_f32_e32 v17, v15, v12
	v_lshlrev_b64 v[12:13], 9, v[88:89]
	v_or_b32_e32 v12, v12, v31
	v_lshl_add_u64 v[14:15], s[74:75], 0, v[12:13]
	global_store_short v[14:15], v86, off
	v_lshl_add_u64 v[14:15], s[76:77], 0, v[12:13]
	v_cvt_pk_bf16_f32 v17, v17, s0
	global_store_short v[14:15], v17, off
	v_lshl_add_u64 v[14:15], s[78:79], 0, v[12:13]
	v_cvt_pk_bf16_f32 v17, v85, s0
	global_store_short v[14:15], v17, off
	v_lshl_add_u64 v[14:15], s[80:81], 0, v[12:13]
	v_cvt_pk_bf16_f32 v17, v16, s0
	v_mul_f32_e32 v10, v10, v16
	global_store_short v[14:15], v17, off
	v_lshl_add_u64 v[14:15], s[82:83], 0, v[12:13]
	v_cvt_pk_bf16_f32 v10, v10, s0
	global_store_short v[14:15], v10, off
	v_lshl_add_u64 v[14:15], s[84:85], 0, v[12:13]
	v_cvt_pk_bf16_f32 v8, v8, s0
	global_store_short v[14:15], v8, off
	v_sub_f32_e32 v8, v130, v83
	v_fma_f32 v8, v8, v2, v83
	v_sub_f32_e32 v10, v111, v83
	v_fmac_f32_e32 v8, v10, v4
	v_mul_f32_e32 v10, v8, v3
	v_mul_f32_e32 v7, 0xbf1b459e, v7
	v_mul_f32_e32 v14, v10, v10
	v_mul_f32_e32 v7, 0x3fb8aa3b, v7
	s_nop 1
	v_mov_b32_dpp v14, v14 quad_perm:[1,0,3,2] row_mask:0xf bank_mask:0xf
	v_exp_f32_e32 v7, v7
	v_lshl_add_u64 v[12:13], s[86:87], 0, v[12:13]
	v_mul_f32_e32 v11, 0xbfb8aa3b, v11
	v_exp_f32_e32 v11, v11
	v_cvt_pk_bf16_f32 v7, v7, s0
	s_waitcnt lgkmcnt(0)
	v_fmac_f32_e32 v14, v10, v10
	global_store_short v[12:13], v7, off
	s_nop 1
	v_mov_b32_dpp v13, v14 quad_perm:[2,3,0,1] row_mask:0xf bank_mask:0xf
	v_sub_f32_e32 v7, v145, v147
	v_mul_f32_e32 v9, 0xbfb8aa3b, v9
	v_fma_f32 v12, v7, v112, v147
	v_sub_f32_e32 v7, v116, v147
	s_waitcnt lgkmcnt(0)
	v_add_f32_e32 v13, v14, v13
	s_nop 1
	v_mov_b32_dpp v14, v13 row_half_mirror row_mask:0xf bank_mask:0xf
	v_exp_f32_e32 v9, v9
	v_fmac_f32_e32 v12, v7, v110
	v_sub_f32_e32 v7, v146, v148
	v_fma_f32 v15, v7, v108, v148
	s_waitcnt lgkmcnt(0)
	v_add_f32_e32 v13, v13, v14
	s_nop 1
	v_mov_b32_dpp v14, v13 row_mirror row_mask:0xf bank_mask:0xf
	v_sub_f32_e32 v7, v114, v148
	v_fmac_f32_e32 v15, v7, v5
	v_add_f32_e32 v7, 1.0, v11
	v_add_f32_e32 v9, 1.0, v9
	s_waitcnt lgkmcnt(0)
	v_add_f32_e32 v11, v13, v14
	v_mov_b32_e32 v13, v11
	s_nop 1
	v_permlane16_swap_b32_e32 v13, v11
	v_rcp_f32_e32 v9, v9
	v_mul_f32_e32 v6, 0xbfb8aa3b, v6
	v_exp_f32_e32 v6, v6
	v_rcp_f32_e32 v14, v7
	v_mul_f32_e32 v7, 0xbf1b459e, v9
	s_waitcnt lgkmcnt(0)
	v_add_f32_e32 v9, v11, v13
	v_mov_b32_e32 v11, v9
	s_nop 1
	v_permlane32_swap_b32_e32 v11, v9
	v_add_f32_e32 v6, 1.0, v6
	v_rcp_f32_e32 v6, v6
	v_mul_f32_e32 v7, 0x3fb8aa3b, v7
	v_exp_f32_e32 v13, v7
	s_waitcnt lgkmcnt(0)
	v_add_f32_e32 v7, v9, v11
	v_add_f32_e32 v7, 0x2b8cbccc, v7
	v_rsq_f32_e32 v7, v7
	v_mul_f32_e32 v6, 0xbf1b459e, v6
	v_mul_f32_e32 v6, 0x3fb8aa3b, v6
	v_exp_f32_e32 v11, v6
	v_add_f32_e32 v6, -1.0, v14
	v_fma_f32 v6, v6, v81, 1.0
	v_ashrrev_i32_e32 v85, 31, v84
	v_mul_f32_e32 v10, v10, v7
	v_mul_f32_e32 v16, v8, v6
	v_lshlrev_b64 v[6:7], 9, v[84:85]
	v_or_b32_e32 v6, v6, v31
	v_lshl_add_u64 v[8:9], s[74:75], 0, v[6:7]
	v_cvt_pk_bf16_f32 v12, v12, s0
	global_store_short v[8:9], v12, off
	v_lshl_add_u64 v[8:9], s[76:77], 0, v[6:7]
	v_cvt_pk_bf16_f32 v12, v16, s0
	global_store_short v[8:9], v12, off
	v_lshl_add_u64 v[8:9], s[78:79], 0, v[6:7]
	v_cvt_pk_bf16_f32 v12, v15, s0
	global_store_short v[8:9], v12, off
	v_lshl_add_u64 v[8:9], s[80:81], 0, v[6:7]
	v_cvt_pk_bf16_f32 v12, v10, s0
	v_mul_f32_e32 v10, v14, v10
	global_store_short v[8:9], v12, off
	v_lshl_add_u64 v[8:9], s[82:83], 0, v[6:7]
	v_cvt_pk_bf16_f32 v10, v10, s0
	global_store_short v[8:9], v10, off
	v_lshl_add_u64 v[8:9], s[84:85], 0, v[6:7]
	v_cvt_pk_bf16_f32 v10, v13, s0
	global_store_short v[8:9], v10, off
	v_sub_f32_e32 v9, v83, v111
	v_fma_f32 v9, v9, v2, v111
	v_sub_f32_e32 v10, v34, v111
	v_fmac_f32_e32 v9, v10, v4
	v_mul_f32_e32 v10, v9, v3
	v_cvt_pk_bf16_f32 v8, v11, s0
	v_mul_f32_e32 v11, v10, v10
	s_nop 1
	v_mov_b32_dpp v11, v11 quad_perm:[1,0,3,2] row_mask:0xf bank_mask:0xf
	v_lshl_add_u64 v[6:7], s[86:87], 0, v[6:7]
	global_store_short v[6:7], v8, off
	v_mul_f32_e32 v14, 0xbfb8aa3b, v94
	v_sub_f32_e32 v6, v147, v116
	s_waitcnt lgkmcnt(0)
	v_fmac_f32_e32 v11, v10, v10
	s_nop 1
	v_mov_b32_dpp v7, v11 quad_perm:[2,3,0,1] row_mask:0xf bank_mask:0xf
	v_exp_f32_e32 v14, v14
	v_fma_f32 v12, v6, v112, v116
	v_sub_f32_e32 v6, v109, v116
	v_fmac_f32_e32 v12, v6, v110
	s_waitcnt lgkmcnt(0)
	v_add_f32_e32 v7, v11, v7
	s_nop 1
	v_mov_b32_dpp v8, v7 row_half_mirror row_mask:0xf bank_mask:0xf
	v_mul_f32_e32 v11, 0xbfb8aa3b, v96
	v_exp_f32_e32 v11, v11
	v_sub_f32_e32 v6, v148, v114
	v_fma_f32 v13, v6, v108, v114
	s_waitcnt lgkmcnt(0)
	v_add_f32_e32 v7, v7, v8
	s_nop 1
	v_mov_b32_dpp v8, v7 row_mirror row_mask:0xf bank_mask:0xf
	v_sub_f32_e32 v6, v79, v114
	v_fmac_f32_e32 v13, v6, v5
	v_add_f32_e32 v6, 1.0, v11
	v_add_f32_e32 v11, 1.0, v14
	v_rcp_f32_e32 v11, v11
	s_waitcnt lgkmcnt(0)
	v_add_f32_e32 v7, v7, v8
	v_mov_b32_e32 v8, v7
	s_nop 1
	v_permlane16_swap_b32_e32 v8, v7
	v_rcp_f32_e32 v14, v6
	v_mul_f32_e32 v6, 0xbf1b459e, v11
	v_mul_f32_e32 v11, 0xbfb8aa3b, v91
	v_exp_f32_e32 v11, v11
	s_waitcnt lgkmcnt(0)
	v_add_f32_e32 v7, v7, v8
	v_mov_b32_e32 v8, v7
	s_nop 1
	v_permlane32_swap_b32_e32 v8, v7
	v_mul_f32_e32 v6, 0x3fb8aa3b, v6
	v_exp_f32_e32 v15, v6
	v_add_f32_e32 v6, 1.0, v11
	v_rcp_f32_e32 v6, v6
	s_waitcnt lgkmcnt(0)
	v_add_f32_e32 v7, v7, v8
	v_add_f32_e32 v7, 0x2b8cbccc, v7
	v_rsq_f32_e32 v7, v7
	v_mul_f32_e32 v6, 0xbf1b459e, v6
	v_mul_f32_e32 v6, 0x3fb8aa3b, v6
	v_exp_f32_e32 v11, v6
	v_add_f32_e32 v6, -1.0, v14
	v_fma_f32 v6, v6, v81, 1.0
	v_ashrrev_i32_e32 v83, 31, v82
	v_mul_f32_e32 v10, v10, v7
	v_mul_f32_e32 v16, v9, v6
	v_lshlrev_b64 v[6:7], 9, v[82:83]
	v_or_b32_e32 v6, v6, v31
	v_lshl_add_u64 v[8:9], s[74:75], 0, v[6:7]
	v_cvt_pk_bf16_f32 v12, v12, s0
	global_store_short v[8:9], v12, off
	v_lshl_add_u64 v[8:9], s[76:77], 0, v[6:7]
	v_cvt_pk_bf16_f32 v12, v16, s0
	global_store_short v[8:9], v12, off
	v_lshl_add_u64 v[8:9], s[78:79], 0, v[6:7]
	v_cvt_pk_bf16_f32 v12, v13, s0
	global_store_short v[8:9], v12, off
	v_lshl_add_u64 v[8:9], s[80:81], 0, v[6:7]
	v_cvt_pk_bf16_f32 v12, v10, s0
	v_mul_f32_e32 v10, v14, v10
	global_store_short v[8:9], v12, off
	v_lshl_add_u64 v[8:9], s[82:83], 0, v[6:7]
	v_cvt_pk_bf16_f32 v10, v10, s0
	global_store_short v[8:9], v10, off
	v_lshl_add_u64 v[8:9], s[84:85], 0, v[6:7]
	v_cvt_pk_bf16_f32 v10, v15, s0
	global_store_short v[8:9], v10, off
	v_lshl_add_u64 v[6:7], s[86:87], 0, v[6:7]
	v_cvt_pk_bf16_f32 v8, v11, s0
	v_cndmask_b32_e64 v113, 0, v113, s[50:51]
	global_store_short v[6:7], v8, off
	v_sub_f32_e32 v6, v111, v34
	v_sub_f32_e32 v7, v113, v34
	v_fmac_f32_e32 v34, v6, v2
	v_fmac_f32_e32 v34, v7, v4
	v_mul_f32_e32 v2, v34, v3
	v_mul_f32_e32 v3, v2, v2
	s_nop 1
	v_mov_b32_dpp v3, v3 quad_perm:[1,0,3,2] row_mask:0xf bank_mask:0xf
	global_load_dword v122, v[44:45], off
	v_sub_f32_e32 v4, v116, v109
	v_sub_f32_e32 v6, v117, v109
	v_fmac_f32_e32 v109, v4, v112
	s_waitcnt lgkmcnt(0)
	v_fmac_f32_e32 v3, v2, v2
	s_nop 1
	v_mov_b32_dpp v4, v3 quad_perm:[2,3,0,1] row_mask:0xf bank_mask:0xf
	v_fmac_f32_e32 v109, v6, v110
	v_sub_f32_e32 v6, v114, v79
	v_sub_f32_e32 v7, v115, v79
	v_fmac_f32_e32 v79, v6, v108
	s_waitcnt lgkmcnt(0)
	v_add_f32_e32 v3, v3, v4
	s_nop 1
	v_mov_b32_dpp v4, v3 row_half_mirror row_mask:0xf bank_mask:0xf
	v_mul_f32_e32 v6, 0xbfb8aa3b, v97
	v_mul_f32_e32 v8, 0xbfb8aa3b, v95
	v_exp_f32_e32 v6, v6
	v_exp_f32_e32 v8, v8
	s_waitcnt lgkmcnt(0)
	v_add_f32_e32 v3, v3, v4
	s_nop 1
	v_mov_b32_dpp v4, v3 row_mirror row_mask:0xf bank_mask:0xf
	v_fmac_f32_e32 v79, v7, v5
	v_add_f32_e32 v5, 1.0, v6
	v_add_f32_e32 v6, 1.0, v8
	v_rcp_f32_e32 v6, v6
	s_waitcnt lgkmcnt(0)
	v_add_f32_e32 v3, v3, v4
	v_mov_b32_e32 v4, v3
	s_nop 1
	v_permlane16_swap_b32_e32 v4, v3
	v_rcp_f32_e32 v7, v5
	v_mul_f32_e32 v5, 0xbf1b459e, v6
	v_mul_f32_e32 v6, 0xbfb8aa3b, v90
	v_exp_f32_e32 v6, v6
	s_waitcnt lgkmcnt(0)
	v_add_f32_e32 v3, v3, v4
	v_mov_b32_e32 v4, v3
	s_nop 1
	v_permlane32_swap_b32_e32 v4, v3
	v_mul_f32_e32 v5, 0x3fb8aa3b, v5
	v_exp_f32_e32 v8, v5
	v_add_f32_e32 v5, 1.0, v6
	v_rcp_f32_e32 v5, v5
	s_waitcnt lgkmcnt(0)
	v_add_f32_e32 v3, v3, v4
	v_add_f32_e32 v3, 0x2b8cbccc, v3
	v_rsq_f32_e32 v3, v3
	v_mul_f32_e32 v4, 0xbf1b459e, v5
	v_mul_f32_e32 v4, 0x3fb8aa3b, v4
	v_exp_f32_e32 v6, v4
	v_mul_f32_e32 v9, v2, v3
	v_add_f32_e32 v2, -1.0, v7
	v_fma_f32 v2, v2, v81, 1.0
	v_ashrrev_i32_e32 v81, 31, v80
	v_mul_f32_e32 v10, v34, v2
	v_lshlrev_b64 v[2:3], 9, v[80:81]
	v_or_b32_e32 v2, v2, v31
	v_lshl_add_u64 v[4:5], s[74:75], 0, v[2:3]
	v_cvt_pk_bf16_f32 v11, v109, s0
	global_store_short v[4:5], v11, off
	v_lshl_add_u64 v[4:5], s[76:77], 0, v[2:3]
	v_cvt_pk_bf16_f32 v10, v10, s0
	global_store_short v[4:5], v10, off
	v_lshl_add_u64 v[4:5], s[78:79], 0, v[2:3]
	v_cvt_pk_bf16_f32 v10, v79, s0
	global_store_short v[4:5], v10, off
	v_lshl_add_u64 v[4:5], s[80:81], 0, v[2:3]
	v_cvt_pk_bf16_f32 v10, v9, s0
	v_mul_f32_e32 v7, v7, v9
	global_store_short v[4:5], v10, off
	v_lshl_add_u64 v[4:5], s[82:83], 0, v[2:3]
	v_cvt_pk_bf16_f32 v7, v7, s0
	global_store_short v[4:5], v7, off
	v_lshl_add_u64 v[4:5], s[84:85], 0, v[2:3]
	v_cvt_pk_bf16_f32 v7, v8, s0
	global_store_short v[4:5], v7, off
	v_lshl_add_u64 v[2:3], s[86:87], 0, v[2:3]
	v_cvt_pk_bf16_f32 v4, v6, s0
	global_store_short v[2:3], v4, off
	ds_read2st64_b32 v[116:117], v141 offset1:2
	ds_read_b128 v[2:5], v142 offset:384
	ds_read2st64_b32 v[118:119], v141 offset0:4 offset1:6
	ds_read_b128 v[6:9], v142 offset:400
	ds_read_b128 v[10:13], v142 offset:416
	ds_read_b128 v[14:17], v142 offset:432
	ds_read_b128 v[80:83], v142 offset:896
	s_waitcnt lgkmcnt(5)
	v_mul_f32_e32 v3, v117, v3
	v_fmac_f32_e32 v3, v116, v2
	s_waitcnt lgkmcnt(4)
	v_mul_f32_e32 v2, v119, v5
	v_fmac_f32_e32 v2, v118, v4
	ds_read_b128 v[84:87], v142 offset:1408
	v_add_f32_e32 v2, v3, v2
	ds_read_b128 v[88:91], v142 offset:1920
	ds_read_b128 v[92:95], v142 offset:2432
	ds_read_b128 v[96:99], v142 offset:2944
	s_waitcnt vmcnt(7)
	v_add_f32_e32 v34, v122, v2
	ds_read_b128 v[2:5], v142 offset:912
	s_waitcnt lgkmcnt(5)
	v_mul_f32_e32 v79, v117, v81
	v_fmac_f32_e32 v79, v116, v80
	v_mul_f32_e32 v80, v119, v83
	v_fmac_f32_e32 v80, v118, v82
	v_add_f32_e32 v79, v79, v80
	ds_read_b128 v[80:83], v142 offset:1424
	s_waitcnt lgkmcnt(5)
	v_mul_f32_e32 v85, v117, v85
	v_fmac_f32_e32 v85, v116, v84
	v_mul_f32_e32 v84, v119, v87
	v_fmac_f32_e32 v84, v118, v86
	v_add_f32_e32 v84, v85, v84
	v_add_f32_e32 v120, v122, v84
	ds_read_b128 v[84:87], v142 offset:1936
	s_waitcnt lgkmcnt(5)
	v_mul_f32_e32 v89, v117, v89
	v_fmac_f32_e32 v89, v116, v88
	v_mul_f32_e32 v88, v119, v91
	v_fmac_f32_e32 v88, v118, v90
	v_add_f32_e32 v88, v89, v88
	v_add_f32_e32 v121, v122, v88
	ds_read_b128 v[88:91], v142 offset:2448
	s_waitcnt lgkmcnt(5)
	v_mul_f32_e32 v93, v117, v93
	v_fmac_f32_e32 v93, v116, v92
	v_mul_f32_e32 v92, v119, v95
	v_fmac_f32_e32 v92, v118, v94
	v_add_f32_e32 v92, v93, v92
	ds_read_b128 v[100:103], v142 offset:3456
	v_add_f32_e32 v123, v122, v92
	ds_read_b128 v[92:95], v142 offset:2960
	s_waitcnt lgkmcnt(6)
	v_mul_f32_e32 v97, v117, v97
	v_fmac_f32_e32 v97, v116, v96
	v_mul_f32_e32 v96, v119, v99
	v_fmac_f32_e32 v96, v118, v98
	v_add_f32_e32 v96, v97, v96
	v_add_f32_e32 v124, v122, v96
	ds_read_b128 v[96:99], v142 offset:3472
	s_waitcnt lgkmcnt(2)
	v_mul_f32_e32 v101, v117, v101
	v_fmac_f32_e32 v101, v116, v100
	v_mul_f32_e32 v100, v119, v103
	v_fmac_f32_e32 v100, v118, v102
	v_add_f32_e32 v104, v101, v100
	ds_read_b128 v[100:103], v143 offset:384
	v_add_f32_e32 v125, v122, v104
	ds_read_b128 v[104:107], v143 offset:400
	ds_read_b128 v[108:111], v143 offset:416
	ds_read_b128 v[112:115], v143 offset:432
	v_add_f32_e32 v79, v122, v79
	s_mov_b32 s2, 0xbfb8aa3b
	s_waitcnt lgkmcnt(3)
	v_mul_f32_e32 v117, v117, v101
	v_fmac_f32_e32 v117, v116, v100
	v_mul_f32_e32 v116, v119, v103
	ds_read2st64_b32 v[100:101], v141 offset0:8 offset1:10
	v_fmac_f32_e32 v116, v118, v102
	ds_read2st64_b32 v[102:103], v141 offset0:12 offset1:14
	v_add_f32_e32 v116, v117, v116
	v_add_f32_e32 v116, v122, v116
	s_waitcnt lgkmcnt(1)
	v_mul_f32_e32 v7, v101, v7
	v_mul_f32_e32 v3, v101, v3
	v_fmac_f32_e32 v7, v100, v6
	s_waitcnt lgkmcnt(0)
	v_mul_f32_e32 v6, v103, v9
	v_fmac_f32_e32 v3, v100, v2
	v_mul_f32_e32 v2, v103, v5
	v_fmac_f32_e32 v6, v102, v8
	v_fmac_f32_e32 v2, v102, v4
	v_add_f32_e32 v6, v7, v6
	v_add_f32_e32 v2, v3, v2
	v_add_f32_e32 v6, v34, v6
	v_add_f32_e32 v34, v79, v2
	v_mul_f32_e32 v2, v101, v81
	v_mul_f32_e32 v3, v103, v83
	v_fmac_f32_e32 v2, v100, v80
	v_fmac_f32_e32 v3, v102, v82
	v_add_f32_e32 v2, v2, v3
	v_add_f32_e32 v79, v120, v2
	v_mul_f32_e32 v2, v101, v85
	v_mul_f32_e32 v3, v103, v87
	v_fmac_f32_e32 v2, v100, v84
	v_fmac_f32_e32 v3, v102, v86
	v_add_f32_e32 v2, v2, v3
	v_add_f32_e32 v117, v121, v2
	v_mul_f32_e32 v2, v101, v89
	v_mul_f32_e32 v3, v103, v91
	v_fmac_f32_e32 v2, v100, v88
	v_fmac_f32_e32 v3, v102, v90
	v_add_f32_e32 v2, v2, v3
	v_add_f32_e32 v118, v123, v2
	v_mul_f32_e32 v2, v101, v93
	v_mul_f32_e32 v3, v103, v95
	v_fmac_f32_e32 v2, v100, v92
	v_fmac_f32_e32 v3, v102, v94
	v_add_f32_e32 v2, v2, v3
	v_add_f32_e32 v119, v124, v2
	v_mul_f32_e32 v2, v101, v97
	v_mul_f32_e32 v3, v103, v99
	v_fmac_f32_e32 v2, v100, v96
	v_fmac_f32_e32 v3, v102, v98
	v_add_f32_e32 v2, v2, v3
	ds_read2st64_b32 v[96:97], v141 offset0:16 offset1:18
	ds_read2st64_b32 v[98:99], v141 offset0:20 offset1:22
	v_add_f32_e32 v120, v125, v2
	v_mul_f32_e32 v2, v101, v105
	v_mul_f32_e32 v3, v103, v107
	v_fmac_f32_e32 v2, v100, v104
	v_fmac_f32_e32 v3, v102, v106
	v_add_f32_e32 v2, v2, v3
	v_add_f32_e32 v100, v116, v2
	ds_read_b128 v[2:5], v142 offset:928
	s_waitcnt lgkmcnt(2)
	v_mul_f32_e32 v7, v97, v11
	s_waitcnt lgkmcnt(1)
	v_mul_f32_e32 v8, v99, v13
	v_fmac_f32_e32 v7, v96, v10
	v_fmac_f32_e32 v8, v98, v12
	v_add_f32_e32 v7, v7, v8
	v_add_f32_e32 v101, v6, v7
	ds_read_b128 v[6:9], v142 offset:1440
	ds_read_b128 v[10:13], v142 offset:944
	s_waitcnt lgkmcnt(2)
	v_mul_f32_e32 v3, v97, v3
	v_fmac_f32_e32 v3, v96, v2
	v_mul_f32_e32 v2, v99, v5
	v_fmac_f32_e32 v2, v98, v4
	v_add_f32_e32 v2, v3, v2
	v_add_f32_e32 v34, v34, v2
	ds_read_b128 v[2:5], v142 offset:1456
	s_waitcnt lgkmcnt(2)
	v_mul_f32_e32 v7, v97, v7
	ds_read_b128 v[80:83], v142 offset:1952
	ds_read_b128 v[84:87], v142 offset:1968
	v_fmac_f32_e32 v7, v96, v6
	v_mul_f32_e32 v6, v99, v9
	v_fmac_f32_e32 v6, v98, v8
	v_add_f32_e32 v6, v7, v6
	v_add_f32_e32 v79, v79, v6
	ds_read_b128 v[6:9], v142 offset:2464
	s_waitcnt lgkmcnt(2)
	v_mul_f32_e32 v81, v97, v81
	v_fmac_f32_e32 v81, v96, v80
	v_mul_f32_e32 v80, v99, v83
	v_fmac_f32_e32 v80, v98, v82
	v_add_f32_e32 v80, v81, v80
	v_add_f32_e32 v102, v117, v80
	ds_read_b128 v[80:83], v142 offset:2480
	s_waitcnt lgkmcnt(1)
	v_mul_f32_e32 v7, v97, v7
	ds_read_b128 v[88:91], v142 offset:2976
	ds_read_b128 v[92:95], v142 offset:2992
	v_fmac_f32_e32 v7, v96, v6
	v_mul_f32_e32 v6, v99, v9
	v_fmac_f32_e32 v6, v98, v8
	v_add_f32_e32 v6, v7, v6
	v_add_f32_e32 v103, v118, v6
	ds_read_b128 v[6:9], v142 offset:3488
	s_waitcnt lgkmcnt(2)
	v_mul_f32_e32 v89, v97, v89
	v_fmac_f32_e32 v89, v96, v88
	v_mul_f32_e32 v88, v99, v91
	v_fmac_f32_e32 v88, v98, v90
	v_add_f32_e32 v88, v89, v88
	v_add_f32_e32 v104, v119, v88
	ds_read_b128 v[88:91], v142 offset:3504
	s_waitcnt lgkmcnt(1)
	v_mul_f32_e32 v7, v97, v7
	v_fmac_f32_e32 v7, v96, v6
	v_mul_f32_e32 v6, v99, v9
	v_fmac_f32_e32 v6, v98, v8
	v_add_f32_e32 v6, v7, v6
	v_add_f32_e32 v105, v120, v6
	v_mul_f32_e32 v6, v97, v109
	v_mul_f32_e32 v7, v99, v111
	v_fmac_f32_e32 v6, v96, v108
	ds_read2st64_b32 v[96:97], v141 offset0:24 offset1:26
	v_fmac_f32_e32 v7, v98, v110
	ds_read2st64_b32 v[98:99], v141 offset0:28 offset1:30
	v_add_f32_e32 v6, v6, v7
	v_add_f32_e32 v100, v100, v6
	s_waitcnt lgkmcnt(1)
	v_mul_f32_e32 v6, v97, v15
	v_fmac_f32_e32 v6, v96, v14
	s_waitcnt lgkmcnt(0)
	v_mul_f32_e32 v7, v99, v17
	v_fmac_f32_e32 v7, v98, v16
	v_mul_f32_e32 v3, v97, v3
	v_add_f32_e32 v6, v6, v7
	v_fmac_f32_e32 v3, v96, v2
	v_mul_f32_e32 v2, v99, v5
	v_add_f32_e32 v9, v101, v6
	v_mul_f32_e32 v6, v97, v11
	v_mul_f32_e32 v7, v99, v13
	v_fmac_f32_e32 v2, v98, v4
	v_fmac_f32_e32 v6, v96, v10
	v_fmac_f32_e32 v7, v98, v12
	v_add_f32_e32 v2, v3, v2
	v_add_f32_e32 v6, v6, v7
	v_add_f32_e32 v7, v79, v2
	v_mul_f32_e32 v2, v97, v85
	v_mul_f32_e32 v3, v99, v87
	v_fmac_f32_e32 v2, v96, v84
	v_fmac_f32_e32 v3, v98, v86
	v_add_f32_e32 v2, v2, v3
	v_add_f32_e32 v8, v34, v6
	v_add_f32_e32 v6, v102, v2
	v_mul_f32_e32 v2, v97, v81
	v_mul_f32_e32 v3, v99, v83
	v_fmac_f32_e32 v2, v96, v80
	v_fmac_f32_e32 v3, v98, v82
	v_add_f32_e32 v2, v2, v3
	v_add_f32_e32 v5, v103, v2
	v_mul_f32_e32 v2, v97, v93
	v_mul_f32_e32 v3, v99, v95
	v_fmac_f32_e32 v2, v96, v92
	v_fmac_f32_e32 v3, v98, v94
	v_add_f32_e32 v2, v2, v3
	v_mul_f32_e64 v11, |v9|, s2
	v_add_f32_e32 v3, v104, v2
	v_mul_f32_e32 v2, v97, v89
	v_mul_f32_e32 v4, v99, v91
	v_exp_f32_e32 v11, v11
	v_fmac_f32_e32 v2, v96, v88
	v_fmac_f32_e32 v4, v98, v90
	v_add_f32_e32 v2, v2, v4
	v_mul_f32_e32 v4, v97, v113
	v_mul_f32_e32 v10, v99, v115
	v_fmac_f32_e32 v4, v96, v112
	v_fmac_f32_e32 v10, v98, v114
	v_add_f32_e32 v4, v4, v10
	v_add_f32_e32 v10, 1.0, v11
	v_log_f32_e32 v10, v10
	v_max_f32_e64 v9, -v9, 0
	s_ashr_i32 s89, s88, 31
	v_lshl_add_u64 v[12:13], v[46:47], 0, s[88:89]
	v_fmac_f32_e32 v9, 0x3f317218, v10
	v_mul_f32_e64 v10, |v8|, s2
	v_exp_f32_e32 v14, v10
	v_lshlrev_b64 v[10:11], 9, v[12:13]
	v_add_f32_e32 v4, v100, v4
	v_mul_f32_e32 v9, 0xbd800000, v9
	v_lshl_add_u64 v[100:101], v[48:49], 0, v[10:11]
	global_store_dword v[100:101], v9, off
	v_add_f32_e32 v9, 1.0, v14
	v_log_f32_e32 v9, v9
	v_mul_f32_e64 v10, |v7|, s2
	v_exp_f32_e32 v10, v10
	v_max_f32_e64 v8, -v8, 0
	v_fmac_f32_e32 v8, 0x3f317218, v9
	v_mul_f32_e32 v8, 0xbd800000, v8
	global_store_dword v[100:101], v8, off offset:512
	v_add_f32_e32 v8, 1.0, v10
	v_log_f32_e32 v8, v8
	v_mul_f32_e64 v9, |v6|, s2
	v_exp_f32_e32 v9, v9
	v_max_f32_e64 v7, -v7, 0
	v_fmac_f32_e32 v7, 0x3f317218, v8
	v_mul_f32_e32 v7, 0xbd800000, v7
	global_store_dword v[100:101], v7, off offset:1024
	v_add_f32_e32 v7, 1.0, v9
	v_log_f32_e32 v7, v7
	v_mul_f32_e64 v8, |v5|, s2
	v_exp_f32_e32 v8, v8
	v_max_f32_e64 v6, -v6, 0
	v_fmac_f32_e32 v6, 0x3f317218, v7
	v_mul_f32_e32 v6, 0xbd800000, v6
	global_store_dword v[100:101], v6, off offset:1536
	v_add_f32_e32 v6, 1.0, v8
	v_log_f32_e32 v6, v6
	v_mul_f32_e64 v7, |v3|, s2
	v_exp_f32_e32 v7, v7
	v_max_f32_e64 v5, -v5, 0
	v_fmac_f32_e32 v5, 0x3f317218, v6
	v_add_f32_e32 v2, v105, v2
	v_mul_f32_e32 v5, 0xbd800000, v5
	global_store_dword v[100:101], v5, off offset:2048
	v_add_f32_e32 v5, 1.0, v7
	v_mul_f32_e64 v6, |v2|, s2
	v_log_f32_e32 v5, v5
	v_exp_f32_e32 v6, v6
	v_max_f32_e64 v3, -v3, 0
	s_add_i32 s4, s88, -2
	v_fmac_f32_e32 v3, 0x3f317218, v5
	v_add_f32_e32 v5, 1.0, v6
	v_mul_f32_e64 v6, |v4|, s2
	v_exp_f32_e32 v6, v6
	v_log_f32_e32 v5, v5
	v_mul_f32_e32 v3, 0xbd800000, v3
	v_mad_i64_i32 v[102:103], s[2:3], s88, v202, v[76:77]
	s_cmp_ge_i32 s4, s1
	global_store_dword v[100:101], v3, off offset:2560
	v_add_f32_e32 v3, 1.0, v6
	s_cselect_b64 s[2:3], -1, 0
	s_cmp_lt_i32 s4, s0
	v_max_f32_e64 v2, -v2, 0
	v_log_f32_e32 v3, v3
	s_cselect_b64 s[4:5], -1, 0
	v_fmac_f32_e32 v2, 0x3f317218, v5
	s_and_b64 vcc, s[2:3], s[4:5]
	v_mul_f32_e32 v2, 0xbd800000, v2
	s_and_b64 s[2:3], vcc, exec
	global_store_dword v[100:101], v2, off offset:3072
	v_max_f32_e64 v2, -v4, 0
	s_cselect_b32 s3, -1, 0
	s_cselect_b32 s2, 0xffffcc00, 0
	s_add_i32 s4, s88, -1
	v_fmac_f32_e32 v2, 0x3f317218, v3
	s_cmp_ge_i32 s4, s1
	v_mul_f32_e32 v34, 0xbd800000, v2
	v_lshl_add_u64 v[2:3], v[102:103], 0, s[2:3]
	s_cselect_b64 s[2:3], -1, 0
	s_cmp_lt_i32 s4, s0
	s_cselect_b64 s[4:5], -1, 0
	s_and_b64 s[2:3], s[2:3], s[4:5]
	s_and_b64 s[4:5], s[2:3], exec
	s_cselect_b32 s5, -1, 0
	s_cselect_b32 s4, 0xffffe600, 0
	s_cmp_ge_i32 s88, s1
	v_lshl_add_u64 v[4:5], v[102:103], 0, s[4:5]
	s_cselect_b64 s[4:5], -1, 0
	s_cmp_lt_i32 s88, s0
	s_cselect_b64 s[6:7], -1, 0
	s_and_b64 s[4:5], s[4:5], s[6:7]
	s_or_b32 s10, s88, 1
	s_cmp_ge_i32 s10, s1
	s_cselect_b64 s[6:7], -1, 0
	s_cmp_lt_i32 s10, s0
	s_cselect_b64 s[8:9], -1, 0
	s_and_b64 s[40:41], s[6:7], s[8:9]
	s_and_b64 s[6:7], s[40:41], exec
	s_cselect_b32 s6, 0x1a00, 0
	s_mov_b32 s72, 0
	s_or_b32 s14, s88, 2
	s_mov_b32 s73, 1
	s_mov_b32 s7, s72
	s_cmp_ge_i32 s14, s1
	v_lshl_add_u64 v[6:7], v[102:103], 0, s[6:7]
	s_cselect_b64 s[6:7], -1, 0
	s_cmp_lt_i32 s14, s0
	s_cselect_b64 s[8:9], -1, 0
	s_and_b64 s[42:43], s[6:7], s[8:9]
	s_and_b64 s[6:7], s[42:43], exec
	s_cselect_b32 s6, 0x3400, 0
	s_mov_b32 s7, s72
	v_lshl_add_u64 v[8:9], v[102:103], 0, s[6:7]
	s_or_b32 s6, s88, 3
	s_cmp_ge_i32 s6, s1
	s_cselect_b64 s[8:9], -1, 0
	s_cmp_lt_i32 s6, s0
	s_cselect_b64 s[18:19], -1, 0
	s_and_b64 s[44:45], s[8:9], s[18:19]
	s_and_b64 s[8:9], s[44:45], exec
	s_cselect_b32 s8, 0x4e00, 0
	s_mov_b32 s9, s72
	v_lshl_add_u64 v[10:11], v[102:103], 0, s[8:9]
	s_or_b32 s8, s88, 4
	s_cmp_ge_i32 s8, s1
	s_cselect_b64 s[18:19], -1, 0
	s_cmp_lt_i32 s8, s0
	s_cselect_b64 s[22:23], -1, 0
	s_and_b64 s[46:47], s[18:19], s[22:23]
	s_and_b64 s[18:19], s[46:47], exec
	s_cselect_b32 s18, 0x6800, 0
	s_or_b32 s34, s88, 5
	s_mov_b32 s19, s72
	s_cmp_ge_i32 s34, s1
	v_lshl_add_u64 v[12:13], v[102:103], 0, s[18:19]
	s_cselect_b64 s[18:19], -1, 0
	s_cmp_lt_i32 s34, s0
	s_cselect_b64 s[22:23], -1, 0
	s_and_b64 s[48:49], s[18:19], s[22:23]
	s_and_b64 s[18:19], s[48:49], exec
	s_cselect_b32 s18, 0x8200, 0
	s_or_b32 s36, s88, 6
	s_mov_b32 s19, s72
	s_cmp_ge_i32 s36, s1
	v_lshl_add_u64 v[14:15], v[102:103], 0, s[18:19]
	s_cselect_b64 s[18:19], -1, 0
	s_cmp_lt_i32 s36, s0
	s_cselect_b64 s[22:23], -1, 0
	s_and_b64 s[50:51], s[18:19], s[22:23]
	s_and_b64 s[18:19], s[50:51], exec
	s_cselect_b32 s18, 0x9c00, 0
	s_or_b32 s28, s88, 7
	s_mov_b32 s19, s72
	s_cmp_ge_i32 s28, s1
	v_lshl_add_u64 v[16:17], v[102:103], 0, s[18:19]
	s_cselect_b64 s[18:19], -1, 0
	s_cmp_lt_i32 s28, s0
	s_cselect_b64 s[22:23], -1, 0
	s_and_b64 s[52:53], s[18:19], s[22:23]
	s_and_b64 s[18:19], s[52:53], exec
	s_cselect_b32 s18, 0xb600, 0
	s_or_b32 s30, s88, 8
	s_mov_b32 s19, s72
	s_cmp_ge_i32 s30, s1
	v_lshl_add_u64 v[80:81], v[102:103], 0, s[18:19]
	s_cselect_b64 s[18:19], -1, 0
	s_cmp_lt_i32 s30, s0
	s_cselect_b64 s[22:23], -1, 0
	s_and_b64 s[54:55], s[18:19], s[22:23]
	s_and_b64 s[18:19], s[54:55], exec
	s_cselect_b32 s18, 0xd000, 0
	s_or_b32 s24, s88, 9
	s_mov_b32 s19, s72
	s_cmp_ge_i32 s24, s1
	v_lshl_add_u64 v[82:83], v[102:103], 0, s[18:19]
	s_cselect_b64 s[18:19], -1, 0
	s_cmp_lt_i32 s24, s0
	s_cselect_b64 s[22:23], -1, 0
	s_and_b64 s[56:57], s[18:19], s[22:23]
	s_and_b64 s[18:19], s[56:57], exec
	s_cselect_b32 s18, 0xea00, 0
	s_or_b32 s26, s88, 10
	s_mov_b32 s19, s72
	s_cmp_ge_i32 s26, s1
	v_lshl_add_u64 v[84:85], v[102:103], 0, s[18:19]
	s_cselect_b64 s[18:19], -1, 0
	s_cmp_lt_i32 s26, s0
	s_cselect_b64 s[22:23], -1, 0
	s_and_b64 s[58:59], s[18:19], s[22:23]
	s_and_b64 s[18:19], s[58:59], exec
	s_cselect_b32 s18, 0x10400, 0
	s_mov_b32 s19, s72
	v_lshl_add_u64 v[86:87], v[102:103], 0, s[18:19]
	s_or_b32 s18, s88, 11
	s_cmp_ge_i32 s18, s1
	s_cselect_b64 s[22:23], -1, 0
	s_cmp_lt_i32 s18, s0
	s_cselect_b64 s[60:61], -1, 0
	s_and_b64 s[60:61], s[22:23], s[60:61]
	s_and_b64 s[22:23], s[60:61], exec
	s_cselect_b32 s22, 0x11e00, 0
	s_mov_b32 s23, s72
	v_lshl_add_u64 v[88:89], v[102:103], 0, s[22:23]
	s_or_b32 s22, s88, 12
	s_cmp_ge_i32 s22, s1
	s_cselect_b64 s[62:63], -1, 0
	s_cmp_lt_i32 s22, s0
	s_cselect_b64 s[64:65], -1, 0
	s_and_b64 s[62:63], s[62:63], s[64:65]
	s_and_b64 s[64:65], s[62:63], exec
	s_cselect_b32 s64, 0x13800, 0
	s_or_b32 s92, s88, 13
	s_mov_b32 s65, s72
	s_cmp_ge_i32 s92, s1
	v_lshl_add_u64 v[90:91], v[102:103], 0, s[64:65]
	s_cselect_b64 s[64:65], -1, 0
	s_cmp_lt_i32 s92, s0
	s_cselect_b64 s[66:67], -1, 0
	s_and_b64 s[64:65], s[64:65], s[66:67]
	s_and_b64 s[66:67], s[64:65], exec
	s_cselect_b32 s66, 0x15200, 0
	s_or_b32 s94, s88, 14
	s_mov_b32 s67, s72
	s_cmp_ge_i32 s94, s1
	v_lshl_add_u64 v[92:93], v[102:103], 0, s[66:67]
	s_cselect_b64 s[66:67], -1, 0
	s_cmp_lt_i32 s94, s0
	s_cselect_b64 s[68:69], -1, 0
	s_and_b64 s[66:67], s[66:67], s[68:69]
	s_and_b64 s[68:69], s[66:67], exec
	s_cselect_b32 s68, 0x16c00, 0
	s_or_b32 s90, s88, 15
	s_mov_b32 s69, s72
	s_cmp_ge_i32 s90, s1
	v_lshl_add_u64 v[94:95], v[102:103], 0, s[68:69]
	s_cselect_b64 s[68:69], -1, 0
	s_cmp_lt_i32 s90, s0
	s_cselect_b64 s[70:71], -1, 0
	s_and_b64 s[70:71], s[68:69], s[70:71]
	s_and_b64 s[68:69], s[70:71], exec
	s_cselect_b32 s68, 0x18600, 0
	s_add_i32 s7, s88, 16
	s_mov_b32 s69, s72
	s_cmp_ge_i32 s7, s1
	v_lshl_add_u64 v[96:97], v[102:103], 0, s[68:69]
	s_cselect_b64 s[68:69], -1, 0
	s_cmp_lt_i32 s7, s0
	s_cselect_b64 s[0:1], -1, 0
	s_and_b64 s[68:69], s[68:69], s[0:1]
	s_and_b64 s[0:1], s[68:69], exec
	global_load_ushort v79, v[2:3], off
	global_load_ushort v104, v[4:5], off
	global_load_ushort v105, v[102:103], off
	global_load_ushort v106, v[6:7], off
	global_load_ushort v107, v[8:9], off
	global_load_ushort v108, v[10:11], off
	global_load_ushort v109, v[12:13], off
	s_cselect_b32 s0, 0x1a000, 0
	s_mov_b32 s1, s72
	global_load_ushort v118, v[14:15], off
	global_load_ushort v119, v[16:17], off
	global_load_ushort v120, v[80:81], off
	global_load_ushort v121, v[82:83], off
	global_load_ushort v122, v[84:85], off
	global_load_ushort v123, v[86:87], off
	global_load_ushort v124, v[88:89], off
	global_load_ushort v125, v[90:91], off
	global_load_ushort v126, v[92:93], off
	global_load_ushort v127, v[94:95], off
	global_load_ushort v128, v[96:97], off
	v_lshl_add_u64 v[98:99], v[102:103], 0, s[0:1]
	global_store_dword v[100:101], v34, off offset:3584
	global_load_ushort v129, v[98:99], off
	global_load_dword v117, v[52:53], off
	global_load_dword v116, v[50:51], off
	global_load_dword v133, v[54:55], off
	global_load_dword v134, v[56:57], off
	global_load_dword v136, v[58:59], off
	global_load_ushort v132, v[102:103], off offset:1024
	s_lshl_b64 s[0:1], s[88:89], 11
	s_ashr_i32 s11, s10, 31
	s_ashr_i32 s15, s14, 31
	s_ashr_i32 s7, s6, 31
	s_ashr_i32 s9, s8, 31
	s_ashr_i32 s35, s34, 31
	s_ashr_i32 s37, s36, 31
	s_ashr_i32 s29, s28, 31
	s_ashr_i32 s31, s30, 31
	s_ashr_i32 s25, s24, 31
	s_ashr_i32 s27, s26, 31
	s_ashr_i32 s19, s18, 31
	s_ashr_i32 s23, s22, 31
	s_ashr_i32 s93, s92, 31
	s_ashr_i32 s95, s94, 31
	s_ashr_i32 s91, s90, 31
	s_mov_b32 s97, 0xbfb8aa3b
	s_waitcnt vmcnt(25)
	v_lshlrev_b32_e32 v34, 16, v79
	v_cndmask_b32_e32 v79, 0, v34, vcc
	s_waitcnt vmcnt(24)
	v_lshlrev_b32_e32 v34, 16, v104
	v_cndmask_b32_e64 v115, 0, v34, s[2:3]
	s_waitcnt vmcnt(23)
	v_lshlrev_b32_e32 v34, 16, v105
	v_cndmask_b32_e64 v114, 0, v34, s[4:5]
	s_waitcnt vmcnt(22)
	v_lshlrev_b32_e32 v34, 16, v106
	v_cndmask_b32_e64 v113, 0, v34, s[40:41]
	s_waitcnt vmcnt(21)
	v_lshlrev_b32_e32 v34, 16, v107
	s_waitcnt vmcnt(5)
	v_mul_f32_e32 v101, v117, v115
	s_waitcnt vmcnt(4)
	v_fmac_f32_e32 v101, v116, v79
	v_cndmask_b32_e64 v112, 0, v34, s[42:43]
	v_lshlrev_b32_e32 v34, 16, v108
	s_waitcnt vmcnt(3)
	v_fmac_f32_e32 v101, v133, v114
	v_cndmask_b32_e64 v111, 0, v34, s[44:45]
	v_lshlrev_b32_e32 v34, 16, v109
	s_waitcnt vmcnt(2)
	v_fmac_f32_e32 v101, v134, v113
	v_cndmask_b32_e64 v110, 0, v34, s[46:47]
	v_lshlrev_b32_e32 v34, 16, v118
	s_waitcnt vmcnt(1)
	v_add_f32_e32 v118, v136, v101
	v_mul_f32_e32 v101, 0xbfb8aa3b, v118
	v_cndmask_b32_e64 v109, 0, v34, s[48:49]
	v_lshlrev_b32_e32 v34, 16, v119
	v_exp_f32_e32 v119, v101
	v_cndmask_b32_e64 v108, 0, v34, s[50:51]
	v_lshlrev_b32_e32 v34, 16, v120
	v_mul_f32_e32 v120, v117, v114
	v_fmac_f32_e32 v120, v116, v115
	v_fmac_f32_e32 v120, v133, v113
	v_add_f32_e32 v119, 1.0, v119
	v_fmac_f32_e32 v120, v134, v112
	v_rcp_f32_e32 v119, v119
	v_add_f32_e32 v115, v136, v120
	v_mul_f32_e32 v120, 0xbfb8aa3b, v115
	v_exp_f32_e32 v120, v120
	v_lshlrev_b32_e32 v100, 16, v129
	v_mul_f32_e32 v118, v118, v119
	v_cndmask_b32_e64 v145, 0, v100, s[68:69]
	v_lshl_add_u64 v[100:101], v[60:61], 0, s[0:1]
	v_cvt_pk_bf16_f32 v118, v118, s0
	v_cndmask_b32_e64 v107, 0, v34, s[52:53]
	v_lshlrev_b32_e32 v34, 16, v121
	global_store_short v[100:101], v118, off
	v_add_f32_e32 v118, 1.0, v120
	v_cndmask_b32_e64 v105, 0, v34, s[54:55]
	v_lshlrev_b32_e32 v34, 16, v122
	v_rcp_f32_e32 v118, v118
	v_cndmask_b32_e64 v104, 0, v34, s[56:57]
	v_lshlrev_b32_e32 v34, 16, v123
	v_cndmask_b32_e64 v103, 0, v34, s[58:59]
	v_lshlrev_b32_e32 v34, 16, v124
	v_cndmask_b32_e64 v102, 0, v34, s[60:61]
	v_lshlrev_b32_e32 v34, 16, v125
	v_cndmask_b32_e64 v106, 0, v34, s[62:63]
	v_lshlrev_b32_e32 v34, 16, v126
	s_lshl_b64 s[0:1], s[10:11], 11
	v_mul_f32_e32 v115, v115, v118
	v_cndmask_b32_e64 v138, 0, v34, s[64:65]
	v_lshlrev_b32_e32 v34, 16, v127
	v_lshl_add_u64 v[126:127], v[60:61], 0, s[0:1]
	v_cvt_pk_bf16_f32 v115, v115, s0
	global_store_short v[126:127], v115, off
	v_mul_f32_e32 v115, v117, v113
	v_fmac_f32_e32 v115, v116, v114
	v_fmac_f32_e32 v115, v133, v112
	v_fmac_f32_e32 v115, v134, v111
	v_add_f32_e32 v114, v136, v115
	v_mul_f32_e32 v115, 0xbfb8aa3b, v114
	v_exp_f32_e32 v115, v115
	v_mul_f32_e32 v118, v117, v112
	v_fmac_f32_e32 v118, v116, v113
	v_fmac_f32_e32 v118, v133, v111
	v_add_f32_e32 v115, 1.0, v115
	v_fmac_f32_e32 v118, v134, v110
	v_rcp_f32_e32 v115, v115
	v_add_f32_e32 v113, v136, v118
	v_mul_f32_e32 v118, 0xbfb8aa3b, v113
	v_exp_f32_e32 v118, v118
	s_lshl_b64 s[0:1], s[14:15], 11
	v_mul_f32_e32 v114, v114, v115
	v_lshl_add_u64 v[130:131], v[60:61], 0, s[0:1]
	v_cvt_pk_bf16_f32 v114, v114, s0
	global_store_short v[130:131], v114, off
	v_add_f32_e32 v114, 1.0, v118
	v_rcp_f32_e32 v114, v114
	s_lshl_b64 s[0:1], s[6:7], 11
	v_lshl_add_u64 v[122:123], v[60:61], 0, s[0:1]
	v_cndmask_b32_e64 v140, 0, v34, s[66:67]
	v_mul_f32_e32 v113, v113, v114
	v_cvt_pk_bf16_f32 v113, v113, s0
	global_store_short v[122:123], v113, off
	v_mul_f32_e32 v113, v117, v111
	v_fmac_f32_e32 v113, v116, v112
	v_fmac_f32_e32 v113, v133, v110
	v_fmac_f32_e32 v113, v134, v109
	v_add_f32_e32 v112, v136, v113
	v_mul_f32_e32 v113, 0xbfb8aa3b, v112
	v_exp_f32_e32 v113, v113
	v_mul_f32_e32 v114, v117, v110
	v_fmac_f32_e32 v114, v116, v111
	v_fmac_f32_e32 v114, v133, v109
	v_add_f32_e32 v113, 1.0, v113
	v_fmac_f32_e32 v114, v134, v108
	v_rcp_f32_e32 v113, v113
	v_add_f32_e32 v111, v136, v114
	v_mul_f32_e32 v114, 0xbfb8aa3b, v111
	v_exp_f32_e32 v114, v114
	s_lshl_b64 s[0:1], s[8:9], 11
	v_mul_f32_e32 v112, v112, v113
	v_lshlrev_b32_e32 v34, 16, v128
	v_lshl_add_u64 v[128:129], v[60:61], 0, s[0:1]
	v_cvt_pk_bf16_f32 v112, v112, s0
	global_store_short v[128:129], v112, off
	v_add_f32_e32 v112, 1.0, v114
	v_rcp_f32_e32 v112, v112
	s_lshl_b64 s[0:1], s[34:35], 11
	v_lshl_add_u64 v[118:119], v[60:61], 0, s[0:1]
	v_mul_f32_e32 v146, v117, v106
	v_mul_f32_e32 v111, v111, v112
	v_cvt_pk_bf16_f32 v111, v111, s0
	global_store_short v[118:119], v111, off
	v_mul_f32_e32 v111, v117, v109
	v_fmac_f32_e32 v111, v116, v110
	v_fmac_f32_e32 v111, v133, v108
	v_fmac_f32_e32 v111, v134, v107
	v_add_f32_e32 v110, v136, v111
	v_mul_f32_e32 v111, 0xbfb8aa3b, v110
	v_exp_f32_e32 v111, v111
	v_mul_f32_e32 v112, v117, v108
	v_fmac_f32_e32 v112, v116, v109
	v_fmac_f32_e32 v112, v133, v107
	v_add_f32_e32 v111, 1.0, v111
	v_fmac_f32_e32 v112, v134, v105
	v_rcp_f32_e32 v111, v111
	v_add_f32_e32 v109, v136, v112
	v_mul_f32_e32 v112, 0xbfb8aa3b, v109
	v_exp_f32_e32 v112, v112
	s_lshl_b64 s[0:1], s[36:37], 11
	v_mul_f32_e32 v110, v110, v111
	v_lshl_add_u64 v[124:125], v[60:61], 0, s[0:1]
	v_cvt_pk_bf16_f32 v110, v110, s0
	global_store_short v[124:125], v110, off
	v_add_f32_e32 v110, 1.0, v112
	v_rcp_f32_e32 v110, v110
	s_lshl_b64 s[0:1], s[28:29], 11
	v_lshl_add_u64 v[112:113], v[60:61], 0, s[0:1]
	v_fmac_f32_e32 v146, v116, v102
	v_mul_f32_e32 v109, v109, v110
	v_cvt_pk_bf16_f32 v109, v109, s0
	global_store_short v[112:113], v109, off
	v_mul_f32_e32 v109, v117, v107
	v_fmac_f32_e32 v109, v116, v108
	v_fmac_f32_e32 v109, v133, v105
	v_fmac_f32_e32 v109, v134, v104
	v_add_f32_e32 v108, v136, v109
	v_mul_f32_e32 v109, 0xbfb8aa3b, v108
	v_exp_f32_e32 v109, v109
	v_mul_f32_e32 v110, v117, v105
	v_fmac_f32_e32 v110, v116, v107
	v_fmac_f32_e32 v110, v133, v104
	v_add_f32_e32 v109, 1.0, v109
	v_fmac_f32_e32 v110, v134, v103
	v_rcp_f32_e32 v109, v109
	v_add_f32_e32 v107, v136, v110
	v_mul_f32_e32 v110, 0xbfb8aa3b, v107
	v_exp_f32_e32 v110, v110
	s_lshl_b64 s[0:1], s[30:31], 11
	v_mul_f32_e32 v108, v108, v109
	v_lshl_add_u64 v[120:121], v[60:61], 0, s[0:1]
	v_cvt_pk_bf16_f32 v108, v108, s0
	global_store_short v[120:121], v108, off
	v_add_f32_e32 v108, 1.0, v110
	v_rcp_f32_e32 v110, v108
	s_lshl_b64 s[0:1], s[24:25], 11
	v_lshl_add_u64 v[108:109], v[60:61], 0, s[0:1]
	v_fmac_f32_e32 v146, v133, v138
	v_mul_f32_e32 v107, v107, v110
	v_cvt_pk_bf16_f32 v107, v107, s0
	global_store_short v[108:109], v107, off
	v_mul_f32_e32 v107, v117, v104
	v_fmac_f32_e32 v107, v116, v105
	v_fmac_f32_e32 v107, v133, v103
	v_fmac_f32_e32 v107, v134, v102
	v_add_f32_e32 v105, v136, v107
	v_mul_f32_e32 v110, v117, v103
	v_mul_f32_e32 v107, 0xbfb8aa3b, v105
	v_fmac_f32_e32 v110, v116, v104
	v_exp_f32_e32 v107, v107
	v_fmac_f32_e32 v110, v133, v102
	v_fmac_f32_e32 v110, v134, v106
	v_add_f32_e32 v110, v136, v110
	v_mul_f32_e32 v104, 0xbfb8aa3b, v110
	v_add_f32_e32 v107, 1.0, v107
	v_exp_f32_e32 v104, v104
	v_rcp_f32_e32 v107, v107
	s_lshl_b64 s[0:1], s[26:27], 11
	v_lshl_add_u64 v[114:115], v[60:61], 0, s[0:1]
	v_add_f32_e32 v104, 1.0, v104
	v_mul_f32_e32 v105, v105, v107
	v_rcp_f32_e32 v107, v104
	v_cvt_pk_bf16_f32 v105, v105, s0
	s_lshl_b64 s[0:1], s[18:19], 11
	global_store_short v[114:115], v105, off
	v_mul_f32_e32 v107, v110, v107
	v_lshl_add_u64 v[104:105], v[60:61], 0, s[0:1]
	v_cvt_pk_bf16_f32 v107, v107, s0
	global_store_short v[104:105], v107, off
	v_mul_f32_e32 v107, v117, v102
	v_fmac_f32_e32 v107, v116, v103
	v_fmac_f32_e32 v107, v133, v106
	v_fmac_f32_e32 v107, v134, v138
	v_add_f32_e32 v103, v136, v107
	v_mul_f32_e32 v107, 0xbfb8aa3b, v103
	v_exp_f32_e32 v107, v107
	v_fmac_f32_e32 v146, v134, v140
	v_add_f32_e32 v146, v136, v146
	v_mul_f32_e32 v102, 0xbfb8aa3b, v146
	v_add_f32_e32 v107, 1.0, v107
	v_exp_f32_e32 v102, v102
	v_rcp_f32_e32 v107, v107
	s_lshl_b64 s[0:1], s[22:23], 11
	v_lshl_add_u64 v[110:111], v[60:61], 0, s[0:1]
	v_add_f32_e32 v102, 1.0, v102
	v_mul_f32_e32 v103, v103, v107
	v_rcp_f32_e32 v107, v102
	v_cvt_pk_bf16_f32 v103, v103, s0
	s_lshl_b64 s[0:1], s[92:93], 11
	global_store_short v[110:111], v103, off
	v_mul_f32_e32 v107, v146, v107
	v_lshl_add_u64 v[102:103], v[60:61], 0, s[0:1]
	v_cvt_pk_bf16_f32 v107, v107, s0
	global_store_short v[102:103], v107, off
	v_mul_f32_e32 v107, v117, v138
	v_fmac_f32_e32 v107, v116, v106
	v_mul_f32_e32 v117, v117, v140
	v_cndmask_b32_e64 v144, 0, v34, s[70:71]
	v_fmac_f32_e32 v107, v133, v140
	v_fmac_f32_e32 v117, v116, v138
	v_fmac_f32_e32 v107, v134, v144
	v_fmac_f32_e32 v117, v133, v144
	v_add_f32_e32 v146, v136, v107
	v_fmac_f32_e32 v117, v134, v145
	v_mul_f32_e32 v106, 0xbfb8aa3b, v146
	v_add_f32_e32 v133, v136, v117
	v_exp_f32_e32 v147, v106
	v_mul_f32_e32 v116, 0xbfb8aa3b, v133
	v_exp_f32_e32 v116, v116
	s_lshl_b64 s[0:1], s[94:95], 11
	v_add_f32_e32 v147, 1.0, v147
	v_rcp_f32_e32 v147, v147
	v_add_f32_e32 v116, 1.0, v116
	v_rcp_f32_e32 v134, v116
	v_lshl_add_u64 v[106:107], v[60:61], 0, s[0:1]
	v_mul_f32_e32 v117, v146, v147
	v_cvt_pk_bf16_f32 v117, v117, s0
	s_lshl_b64 s[0:1], s[90:91], 11
	v_mul_f32_e32 v133, v133, v134
	global_store_short v[106:107], v117, off
	v_lshl_add_u64 v[116:117], v[60:61], 0, s[0:1]
	v_cvt_pk_bf16_f32 v133, v133, s0
	global_load_dword v34, v[50:51], off offset:2048
	global_load_dword v79, v[58:59], off offset:2048
	s_nop 0
	global_store_short v[116:117], v133, off
	global_load_ushort v2, v[2:3], off offset:1024
	s_nop 0
	global_load_ushort v3, v[4:5], off offset:1024
	s_nop 0
	global_load_ushort v4, v[6:7], off offset:1024
	global_load_ushort v5, v[8:9], off offset:1024
	s_nop 0
	global_load_ushort v6, v[10:11], off offset:1024
	global_load_ushort v7, v[12:13], off offset:1024
	global_load_ushort v8, v[14:15], off offset:1024
	global_load_ushort v9, v[16:17], off offset:1024
	s_nop 0
	global_load_ushort v10, v[80:81], off offset:1024
	global_load_ushort v11, v[82:83], off offset:1024
	global_load_ushort v12, v[84:85], off offset:1024
	global_load_ushort v13, v[86:87], off offset:1024
	global_load_ushort v14, v[88:89], off offset:1024
	global_load_ushort v15, v[90:91], off offset:1024
	global_load_ushort v16, v[92:93], off offset:1024
	global_load_ushort v17, v[94:95], off offset:1024
	global_load_ushort v80, v[96:97], off offset:1024
	global_load_ushort v81, v[98:99], off offset:1024
	global_load_dword v82, v[62:63], off
	global_load_dword v83, v[64:65], off
	global_load_dword v84, v[66:67], off
	s_waitcnt vmcnt(39)
	v_lshlrev_b32_e32 v85, 16, v132
	v_cndmask_b32_e64 v85, 0, v85, s[4:5]
	s_waitcnt vmcnt(20)
	v_lshlrev_b32_e32 v2, 16, v2
	s_waitcnt vmcnt(19)
	v_lshlrev_b32_e32 v3, 16, v3
	v_cndmask_b32_e64 v3, 0, v3, s[2:3]
	v_cndmask_b32_e32 v2, 0, v2, vcc
	s_waitcnt vmcnt(18)
	v_lshlrev_b32_e32 v4, 16, v4
	v_cndmask_b32_e64 v4, 0, v4, s[40:41]
	s_waitcnt vmcnt(17)
	v_lshlrev_b32_e32 v5, 16, v5
	v_cndmask_b32_e64 v5, 0, v5, s[42:43]
	s_waitcnt vmcnt(16)
	v_lshlrev_b32_e32 v6, 16, v6
	v_cndmask_b32_e64 v6, 0, v6, s[44:45]
	s_waitcnt vmcnt(15)
	v_lshlrev_b32_e32 v7, 16, v7
	v_cndmask_b32_e64 v7, 0, v7, s[46:47]
	s_waitcnt vmcnt(14)
	v_lshlrev_b32_e32 v8, 16, v8
	v_cndmask_b32_e64 v8, 0, v8, s[48:49]
	s_waitcnt vmcnt(13)
	v_lshlrev_b32_e32 v9, 16, v9
	v_cndmask_b32_e64 v9, 0, v9, s[50:51]
	s_waitcnt vmcnt(12)
	v_lshlrev_b32_e32 v10, 16, v10
	v_cndmask_b32_e64 v10, 0, v10, s[52:53]
	s_waitcnt vmcnt(2)
	v_mul_f32_e32 v86, v82, v3
	v_fmac_f32_e32 v86, v34, v2
	s_waitcnt vmcnt(1)
	v_fmac_f32_e32 v86, v83, v85
	v_mul_f32_e32 v87, v82, v85
	s_waitcnt vmcnt(0)
	v_fmac_f32_e32 v86, v84, v4
	v_fmac_f32_e32 v87, v34, v3
	v_add_f32_e32 v2, v79, v86
	v_fmac_f32_e32 v87, v83, v4
	v_mul_f32_e32 v86, 0xbfb8aa3b, v2
	v_fmac_f32_e32 v87, v84, v5
	v_exp_f32_e32 v86, v86
	v_add_f32_e32 v3, v79, v87
	v_mul_f32_e32 v87, 0xbfb8aa3b, v3
	v_exp_f32_e32 v87, v87
	v_add_f32_e32 v86, 1.0, v86
	v_rcp_f32_e32 v86, v86
	v_lshlrev_b32_e32 v11, 16, v11
	v_add_f32_e32 v87, 1.0, v87
	v_rcp_f32_e32 v87, v87
	v_mul_f32_e32 v2, v2, v86
	v_cvt_pk_bf16_f32 v2, v2, s0
	global_store_short v[100:101], v2, off offset:1024
	v_mul_f32_e32 v2, v3, v87
	v_mul_f32_e32 v3, v82, v4
	v_fmac_f32_e32 v3, v34, v85
	v_fmac_f32_e32 v3, v83, v5
	v_fmac_f32_e32 v3, v84, v6
	v_add_f32_e32 v3, v79, v3
	v_mul_f32_e32 v85, 0xbfb8aa3b, v3
	v_exp_f32_e32 v85, v85
	v_mul_f32_e32 v86, v82, v5
	v_fmac_f32_e32 v86, v34, v4
	v_fmac_f32_e32 v86, v83, v6
	v_fmac_f32_e32 v86, v84, v7
	v_add_f32_e32 v85, 1.0, v85
	v_add_f32_e32 v4, v79, v86
	v_rcp_f32_e32 v85, v85
	v_mul_f32_e32 v86, 0xbfb8aa3b, v4
	v_exp_f32_e32 v86, v86
	v_cvt_pk_bf16_f32 v2, v2, s0
	v_mul_f32_e32 v3, v3, v85
	v_cvt_pk_bf16_f32 v3, v3, s0
	global_store_short v[126:127], v2, off offset:1024
	v_add_f32_e32 v2, 1.0, v86
	global_store_short v[130:131], v3, off offset:1024
	v_mul_f32_e32 v3, v82, v6
	v_rcp_f32_e32 v2, v2
	v_fmac_f32_e32 v3, v34, v5
	v_fmac_f32_e32 v3, v83, v7
	v_fmac_f32_e32 v3, v84, v8
	v_add_f32_e32 v3, v79, v3
	v_mul_f32_e32 v2, v4, v2
	v_mul_f32_e32 v4, 0xbfb8aa3b, v3
	v_exp_f32_e32 v4, v4
	v_mul_f32_e32 v5, v82, v7
	v_fmac_f32_e32 v5, v34, v6
	v_fmac_f32_e32 v5, v83, v8
	v_add_f32_e32 v4, 1.0, v4
	v_rcp_f32_e32 v4, v4
	v_fmac_f32_e32 v5, v84, v9
	v_add_f32_e32 v5, v79, v5
	v_mul_f32_e32 v6, 0xbfb8aa3b, v5
	v_mul_f32_e32 v3, v3, v4
	v_exp_f32_e32 v6, v6
	v_cvt_pk_bf16_f32 v3, v3, s0
	global_store_short v[128:129], v3, off offset:1024
	v_mul_f32_e32 v3, v82, v8
	v_fmac_f32_e32 v3, v34, v7
	v_cvt_pk_bf16_f32 v2, v2, s0
	v_fmac_f32_e32 v3, v83, v9
	global_store_short v[122:123], v2, off offset:1024
	v_add_f32_e32 v2, 1.0, v6
	v_fmac_f32_e32 v3, v84, v10
	v_rcp_f32_e32 v2, v2
	v_add_f32_e32 v3, v79, v3
	v_mul_f32_e32 v4, 0xbfb8aa3b, v3
	v_exp_f32_e32 v4, v4
	v_mul_f32_e32 v2, v5, v2
	v_mul_f32_e32 v5, v82, v9
	v_fmac_f32_e32 v5, v34, v8
	v_cndmask_b32_e64 v11, 0, v11, s[54:55]
	v_fmac_f32_e32 v5, v83, v10
	v_add_f32_e32 v4, 1.0, v4
	v_fmac_f32_e32 v5, v84, v11
	v_rcp_f32_e32 v4, v4
	v_add_f32_e32 v5, v79, v5
	v_mul_f32_e32 v6, 0xbfb8aa3b, v5
	v_exp_f32_e32 v6, v6
	v_mul_f32_e32 v3, v3, v4
	v_cvt_pk_bf16_f32 v3, v3, s0
	v_cvt_pk_bf16_f32 v2, v2, s0
	global_store_short v[124:125], v3, off offset:1024
	v_mul_f32_e32 v3, v82, v10
	v_lshlrev_b32_e32 v12, 16, v12
	global_store_short v[118:119], v2, off offset:1024
	v_add_f32_e32 v2, 1.0, v6
	v_fmac_f32_e32 v3, v34, v9
	v_cndmask_b32_e64 v12, 0, v12, s[56:57]
	v_rcp_f32_e32 v2, v2
	v_fmac_f32_e32 v3, v83, v11
	v_fmac_f32_e32 v3, v84, v12
	v_add_f32_e32 v3, v79, v3
	v_mul_f32_e32 v4, 0xbfb8aa3b, v3
	v_mul_f32_e32 v2, v5, v2
	v_exp_f32_e32 v4, v4
	v_mul_f32_e32 v5, v82, v11
	v_lshlrev_b32_e32 v13, 16, v13
	v_fmac_f32_e32 v5, v34, v10
	v_cndmask_b32_e64 v13, 0, v13, s[58:59]
	v_fmac_f32_e32 v5, v83, v12
	v_fmac_f32_e32 v5, v84, v13
	v_add_f32_e32 v5, v79, v5
	v_add_f32_e32 v4, 1.0, v4
	v_mul_f32_e32 v6, 0xbfb8aa3b, v5
	v_rcp_f32_e32 v4, v4
	v_exp_f32_e32 v6, v6
	v_cvt_pk_bf16_f32 v2, v2, s0
	global_store_short v[112:113], v2, off offset:1024
	v_mul_f32_e32 v3, v3, v4
	v_add_f32_e32 v2, 1.0, v6
	v_cvt_pk_bf16_f32 v3, v3, s0
	v_rcp_f32_e32 v2, v2
	global_store_short v[120:121], v3, off offset:1024
	v_mul_f32_e32 v3, v82, v12
	v_lshlrev_b32_e32 v14, 16, v14
	v_fmac_f32_e32 v3, v34, v11
	v_cndmask_b32_e64 v14, 0, v14, s[60:61]
	v_fmac_f32_e32 v3, v83, v13
	v_fmac_f32_e32 v3, v84, v14
	v_mul_f32_e32 v2, v5, v2
	v_add_f32_e32 v3, v79, v3
	v_mul_f32_e32 v5, v82, v13
	v_lshlrev_b32_e32 v15, 16, v15
	v_mul_f32_e32 v4, 0xbfb8aa3b, v3
	v_fmac_f32_e32 v5, v34, v12
	v_cndmask_b32_e64 v15, 0, v15, s[62:63]
	v_exp_f32_e32 v4, v4
	v_fmac_f32_e32 v5, v83, v14
	v_fmac_f32_e32 v5, v84, v15
	v_add_f32_e32 v5, v79, v5
	v_mul_f32_e32 v6, 0xbfb8aa3b, v5
	v_exp_f32_e32 v6, v6
	v_add_f32_e32 v4, 1.0, v4
	v_rcp_f32_e32 v4, v4
	v_cvt_pk_bf16_f32 v2, v2, s0
	global_store_short v[108:109], v2, off offset:1024
	v_add_f32_e32 v2, 1.0, v6
	v_rcp_f32_e32 v2, v2
	v_mul_f32_e32 v3, v3, v4
	v_cvt_pk_bf16_f32 v3, v3, s0
	global_store_short v[114:115], v3, off offset:1024
	v_mul_f32_e32 v3, v82, v14
	v_lshlrev_b32_e32 v16, 16, v16
	v_fmac_f32_e32 v3, v34, v13
	v_cndmask_b32_e64 v16, 0, v16, s[64:65]
	v_mul_f32_e32 v2, v5, v2
	v_fmac_f32_e32 v3, v83, v15
	v_mul_f32_e32 v5, v82, v15
	v_lshlrev_b32_e32 v17, 16, v17
	v_fmac_f32_e32 v3, v84, v16
	v_fmac_f32_e32 v5, v34, v14
	v_cndmask_b32_e64 v17, 0, v17, s[66:67]
	v_add_f32_e32 v3, v79, v3
	v_fmac_f32_e32 v5, v83, v16
	v_mul_f32_e32 v4, 0xbfb8aa3b, v3
	v_fmac_f32_e32 v5, v84, v17
	v_exp_f32_e32 v4, v4
	v_add_f32_e32 v5, v79, v5
	v_mul_f32_e32 v6, 0xbfb8aa3b, v5
	v_exp_f32_e32 v6, v6
	v_add_f32_e32 v4, 1.0, v4
	v_cvt_pk_bf16_f32 v2, v2, s0
	v_rcp_f32_e32 v4, v4
	global_store_short v[104:105], v2, off offset:1024
	v_add_f32_e32 v2, 1.0, v6
	v_rcp_f32_e32 v2, v2
	v_mul_f32_e32 v3, v3, v4
	v_cvt_pk_bf16_f32 v3, v3, s0
	v_lshlrev_b32_e32 v80, 16, v80
	global_store_short v[110:111], v3, off offset:1024
	v_mul_f32_e32 v2, v5, v2
	v_mul_f32_e32 v3, v82, v16
	v_mul_f32_e32 v5, v82, v17
	v_cndmask_b32_e64 v80, 0, v80, s[70:71]
	v_lshlrev_b32_e32 v81, 16, v81
	v_fmac_f32_e32 v3, v34, v15
	v_fmac_f32_e32 v5, v34, v16
	v_cndmask_b32_e64 v81, 0, v81, s[68:69]
	v_fmac_f32_e32 v3, v83, v17
	v_fmac_f32_e32 v5, v83, v80
	v_fmac_f32_e32 v3, v84, v80
	v_fmac_f32_e32 v5, v84, v81
	v_add_f32_e32 v3, v79, v3
	v_add_f32_e32 v5, v79, v5
	v_mul_f32_e32 v4, 0xbfb8aa3b, v3
	v_mul_f32_e32 v6, 0xbfb8aa3b, v5
	v_exp_f32_e32 v4, v4
	v_exp_f32_e32 v6, v6
	v_cvt_pk_bf16_f32 v2, v2, s0
	global_store_short v[102:103], v2, off offset:1024
	v_add_f32_e32 v4, 1.0, v4
	v_add_f32_e32 v2, 1.0, v6
	v_rcp_f32_e32 v4, v4
	v_rcp_f32_e32 v2, v2
	v_mul_f32_e32 v3, v3, v4
	v_mul_f32_e32 v2, v5, v2
	v_cvt_pk_bf16_f32 v3, v3, s0
	v_cvt_pk_bf16_f32 v2, v2, s0
	global_store_short v[106:107], v3, off offset:1024
	global_store_short v[116:117], v2, off offset:1024
	s_and_saveexec_b64 s[0:1], s[38:39]
	s_movk_i32 s90, 0x1a00
	s_cbranch_execz .LBB0_247
	v_readlane_b32 s2, v255, 48
	v_readlane_b32 s3, v255, 49
	v_add_u32_e32 v2, s88, v19
	v_mov_b32_e32 v79, v35
	v_mov_b64_e32 v[4:5], s[2:3]
	v_mad_i64_i32 v[4:5], s[2:3], v2, s90, v[4:5]
	v_lshl_add_u64 v[4:5], v[4:5], 0, v[78:79]
	v_add_co_u32_e32 v4, vcc, 0x1000, v4
	s_nop 1
	v_addc_co_u32_e32 v5, vcc, 0, v5, vcc
	global_load_ushort v3, v[4:5], off offset:2432
	s_nop 0
	global_load_dword v4, v[68:69], off
	s_waitcnt vmcnt(1)
	v_lshlrev_b32_e32 v3, 16, v3
	s_waitcnt vmcnt(0)
	v_add_f32_e32 v4, v4, v3
	v_mul_f32_e64 v3, |v4|, s97
	v_exp_f32_e32 v3, v3
	v_max_f32_e32 v4, 0, v4
	v_add_f32_e32 v3, 1.0, v3
	v_log_f32_e32 v5, v3
	v_ashrrev_i32_e32 v3, 31, v2
	v_lshlrev_b64 v[2:3], 6, v[2:3]
	v_lshl_add_u64 v[2:3], v[70:71], 0, v[2:3]
	v_fmac_f32_e32 v4, 0x3f317218, v5
	global_store_dword v[2:3], v4, off
	s_branch .LBB0_247
